# attention: K/V blocks shared by the 4 waves of a unit through one LDS image per unit (DMA volume /2.5), 2 workgroup barriers per unit, lockstep
# speedup vs baseline: 1.0044x; 1.0044x over previous
.LBB0_420:
	s_ashr_i32 s2, s1, 6
	s_add_u32 s84, s6, 0x8000000
	s_addc_u32 s85, s7, 0
	s_ashr_i32 s4, s1, 8
	s_lshl_b32 s21, s2, 5
	s_lshl_b32 s1, s2, 14
	s_and_b32 s3, s21, 0x60
	s_lshl_b32 s75, s4, 16
	s_lshl_b32 s1, s3, 7
	s_add_i32 s75, s75, s1
	v_and_b32_e32 v8, 63, v4
	s_cmp_gt_i32 s0, 0
	v_and_b32_e32 v7, 31, v4
	v_bfe_u32 v6, v4, 5, 1
	s_mov_b32 s86, 0
	s_mov_b32 s81, 1
	s_cselect_b64 s[8:9], -1, 0
	s_cmp_lt_i32 s0, 1
	v_lshrrev_b32_e32 v5, 3, v8
	v_writelane_b32 v254, s4, 14
	s_cbranch_scc1 .LBB0_428
	s_lshl_b32 s1, s90, 1
	s_add_i32 s1, s4, s1
	s_ashr_i32 s86, s1, 11
	s_bfe_u32 s2, s1, 0x70004
	s_and_b32 s88, s1, 15
	s_lshl_b32 s1, s86, 1
	s_lshr_b32 s33, s2, s1
	s_bfm_b32 s4, s1, 0
	s_and_b32 s2, s4, s2
	s_lshl_b32 s4, s33, 7
	s_or_b32 s12, s21, 0xffffff80
	s_lshl_b32 s4, s4, s1
	v_or_b32_e32 v1, s12, v5
	s_or_b32 s42, s4, s2
	v_lshlrev_b32_e32 v1, s1, v1
	v_add_u32_e32 v1, s42, v1
	s_movk_i32 s2, 0xc40
	v_mul_lo_u32 v1, v1, s2
	s_lshl_b32 s2, s88, 6
	v_bitop3_b32 v2, v5, v4, 7 bitop3:0x78
	v_add_lshl_u32 v1, v1, s2, 1
	v_lshl_or_b32 v2, v2, 4, v1
	s_cmp_lg_u32 s33, 0
	s_cselect_b64 s[10:11], -1, 0
	s_cmp_eq_u32 s33, 0
	v_add_u32_e32 v178, 0x800, v2
	s_cbranch_scc1 .LBB0_504
	v_mov_b32_e32 v179, 0
	v_lshl_add_u64 v[2:3], s[84:85], 0, v[178:179]
	s_lshl_b32 s4, 8, s1
	v_mov_b32_e32 v9, 0x1880
	s_add_i32 m0, s75, 0x2000
	v_mad_i64_i32 v[10:11], s[4:5], s4, v9, v[2:3]
	s_add_i32 m0, s75, 0x2400
	s_lshl_b32 s4, 16, s1
	v_mad_u64_u32 v[10:11], s[4:5], s4, v9, v[2:3]
	s_add_i32 m0, s75, 0x2800
	s_lshl_b32 s4, 24, s1
	v_mad_i64_i32 v[2:3], s[4:5], s4, v9, v[2:3]
	s_cbranch_execnz .LBB0_424
.LBB0_423:
	v_mov_b32_e32 v2, v0
	s_movk_i32 s16, 0x1880
	v_lshrrev_b32_e32 v3, 3, v2
	v_bfe_u32 v9, v2, 3, 3
	v_xor_b32_e32 v12, v3, v2
	v_or_b32_e32 v2, s12, v9
	v_lshlrev_b32_e32 v2, s1, v2
	v_add_u32_e32 v2, s42, v2
	v_max_i32_e32 v10, 0, v2
	v_mov_b64_e32 v[2:3], s[84:85]
	s_mov_b32 s5, 0
	v_mad_u64_u32 v[10:11], s[12:13], v10, s16, v[2:3]
	s_lshl_b32 s4, s2, 1
	v_lshlrev_b32_e32 v12, 4, v12
	v_lshl_add_u64 v[10:11], v[10:11], 0, s[4:5]
	v_and_b32_e32 v12, 0x70, v12
	v_mov_b32_e32 v13, 0
	v_lshl_add_u64 v[10:11], v[10:11], 0, v[12:13]
	s_mov_b64 s[12:13], 0x800
	v_lshl_add_u64 v[10:11], v[10:11], 0, s[12:13]
	s_add_i32 m0, s75, 0x2000
	s_or_b32 s14, s21, 0xffffff88
	v_or_b32_e32 v10, s14, v9
	v_lshlrev_b32_e32 v10, s1, v10
	v_add_u32_e32 v10, s42, v10
	v_max_i32_e32 v10, 0, v10
	v_mad_u64_u32 v[10:11], s[14:15], v10, s16, v[2:3]
	v_lshl_add_u64 v[10:11], v[10:11], 0, s[4:5]
	v_lshl_add_u64 v[10:11], v[10:11], 0, v[12:13]
	v_lshl_add_u64 v[10:11], v[10:11], 0, s[12:13]
	s_add_i32 m0, s75, 0x2400
	s_or_b32 s14, s21, 0xffffff90
	v_or_b32_e32 v10, s14, v9
	v_lshlrev_b32_e32 v10, s1, v10
	v_add_u32_e32 v10, s42, v10
	v_max_i32_e32 v10, 0, v10
	v_mad_u64_u32 v[10:11], s[14:15], v10, s16, v[2:3]
	v_lshl_add_u64 v[10:11], v[10:11], 0, s[4:5]
	v_lshl_add_u64 v[10:11], v[10:11], 0, v[12:13]
	v_lshl_add_u64 v[10:11], v[10:11], 0, s[12:13]
	s_add_i32 m0, s75, 0x2800
	s_or_b32 s14, s21, 0xffffff98
	v_or_b32_e32 v9, s14, v9
	v_lshlrev_b32_e32 v9, s1, v9
	v_add_u32_e32 v9, s42, v9
	v_max_i32_e32 v9, 0, v9
	v_mad_u64_u32 v[2:3], s[14:15], v9, s16, v[2:3]
	v_lshl_add_u64 v[2:3], v[2:3], 0, s[4:5]
	v_lshl_add_u64 v[2:3], v[2:3], 0, v[12:13]
	v_lshl_add_u64 v[2:3], v[2:3], 0, s[12:13]
.LBB0_424:
	s_add_i32 m0, s75, 0x2c00
	s_andn2_b64 vcc, exec, s[10:11]
	s_cbranch_vccnz .LBB0_505
	v_mov_b32_e32 v179, 0
	v_lshl_add_u64 v[2:3], s[84:85], 0, v[178:179]
	s_lshl_b32 s4, 32, s1
	v_mov_b32_e32 v9, 0x1880
	v_mad_i64_i32 v[10:11], s[4:5], s4, v9, v[2:3]
	s_add_i32 m0, s75, 0x3000
	s_lshl_b32 s4, 40, s1
	v_mad_i64_i32 v[10:11], s[4:5], s4, v9, v[2:3]
	s_add_i32 m0, s75, 0x3400
	s_lshl_b32 s4, 48, s1
	v_mad_i64_i32 v[10:11], s[4:5], s4, v9, v[2:3]
	s_add_i32 m0, s75, 0x3800
	s_lshl_b32 s4, 56, s1
	v_mad_i64_i32 v[2:3], s[4:5], s4, v9, v[2:3]
	s_add_i32 m0, s75, 0x3c00
	s_nop 0
	v_and_b32_e32 v2, 7, v4
	s_cbranch_execnz .LBB0_427
.LBB0_426:
	v_mov_b32_e32 v3, v0
	s_add_i32 s4, s3, 0xffffffa0
	v_lshrrev_b32_e32 v9, 3, v3
	v_xor_b32_e32 v3, v9, v3
	v_and_or_b32 v9, v9, 7, s4
	v_lshlrev_b32_e32 v10, s1, v9
	v_add_u32_e32 v10, s42, v10
	v_max_i32_e32 v12, 0, v10
	s_movk_i32 s14, 0x1880
	v_mov_b64_e32 v[10:11], s[84:85]
	v_lshlrev_b32_e32 v3, 4, v3
	s_mov_b32 s5, 0
	v_mad_u64_u32 v[12:13], s[10:11], v12, s14, v[10:11]
	s_lshl_b32 s4, s2, 1
	v_and_b32_e32 v14, 0x70, v3
	v_or_b32_e32 v3, 8, v9
	v_lshl_add_u64 v[12:13], v[12:13], 0, s[4:5]
	v_mov_b32_e32 v15, 0
	v_lshlrev_b32_e32 v3, s1, v3
	v_lshl_add_u64 v[12:13], v[12:13], 0, v[14:15]
	s_mov_b64 s[10:11], 0x800
	v_add_u32_e32 v3, s42, v3
	s_add_i32 m0, s75, 0x3000
	v_lshl_add_u64 v[12:13], v[12:13], 0, s[10:11]
	v_max_i32_e32 v3, 0, v3
	v_mad_u64_u32 v[12:13], s[12:13], v3, s14, v[10:11]
	v_or_b32_e32 v3, 16, v9
	v_lshl_add_u64 v[12:13], v[12:13], 0, s[4:5]
	v_lshlrev_b32_e32 v3, s1, v3
	v_lshl_add_u64 v[12:13], v[12:13], 0, v[14:15]
	v_add_u32_e32 v3, s42, v3
	v_lshl_add_u64 v[12:13], v[12:13], 0, s[10:11]
	s_add_i32 m0, s75, 0x3400
	v_max_i32_e32 v3, 0, v3
	v_mad_u64_u32 v[12:13], s[12:13], v3, s14, v[10:11]
	v_or_b32_e32 v3, 24, v9
	v_lshlrev_b32_e32 v3, s1, v3
	v_add_u32_e32 v3, s42, v3
	v_max_i32_e32 v3, 0, v3
	v_lshl_add_u64 v[12:13], v[12:13], 0, s[4:5]
	v_mad_u64_u32 v[10:11], s[12:13], v3, s14, v[10:11]
	v_lshl_add_u64 v[12:13], v[12:13], 0, v[14:15]
	v_lshl_add_u64 v[10:11], v[10:11], 0, s[4:5]
	v_lshl_add_u64 v[12:13], v[12:13], 0, s[10:11]
	s_add_i32 m0, s75, 0x3800
	v_lshl_add_u64 v[10:11], v[10:11], 0, v[14:15]
	v_lshl_add_u64 v[10:11], v[10:11], 0, s[10:11]
	s_add_i32 m0, s75, 0x3c00
	s_nop 0
.LBB0_427:
	v_or_b32_e32 v3, s3, v7
	v_lshlrev_b32_e32 v3, s1, v3
	v_add_u32_e32 v180, s42, v3
	s_movk_i32 s4, 0x1880
	v_mov_b64_e32 v[10:11], s[84:85]
	v_mad_i64_i32 v[10:11], s[4:5], v180, s4, v[10:11]
	s_lshl_b32 s4, s2, 1
	s_mov_b32 s5, 0
	v_lshl_add_u64 v[10:11], v[10:11], 0, s[4:5]
	v_lshlrev_b32_e32 v12, 4, v6
	v_mov_b32_e32 v13, 0
	v_lshl_add_u64 v[10:11], v[10:11], 0, v[12:13]
	global_load_dwordx4 v[146:149], v[10:11], off offset:96
	global_load_dwordx4 v[150:153], v[10:11], off offset:64
	global_load_dwordx4 v[154:157], v[10:11], off offset:32
	global_load_dwordx4 v[158:161], v[10:11], off
	s_lshl_b32 s81, 1, s1
	s_lshl_b32 s1, 0xffffff80, s1
	s_waitcnt vmcnt(0)
	s_add_i32 s82, s42, s1
	v_lshlrev_b32_e32 v2, 4, v2
	s_movk_i32 s1, 0x1000
	v_add3_u32 v182, v1, v2, s1
	s_movk_i32 s16, 0x1880
	v_and_b32_e32 v100, 63, v0
	v_lshrrev_b32_e32 v101, 3, v100
	v_and_b32_e32 v104, 7, v100
	v_xor_b32_e32 v104, v104, v101
	v_lshlrev_b32_e32 v104, 4, v104
	s_lshl_b32 s10, s88, 7
	s_add_u32 s10, s10, 0x800
	v_add_u32_e32 v104, s10, v104
	v_mov_b32_e32 v105, 0
	v_lshl_add_u64 v[106:107], s[84:85], 0, v[104:105]
	s_bfe_u32 s11, s75, 0x2000c
	s_and_b32 s12, s75, 0xffff0000
	s_add_u32 s12, s12, 0x8000
	s_add_u32 s13, s11, 1
	s_lshl_b32 s10, s13, 5
	v_add_u32_e32 v102, s10, v101
	s_lshl_b32 s10, s13, 12
	s_add_u32 s10, s10, s12
	v_mul_lo_u32 v103, v102, s81
	v_add_u32_e32 v103, s82, v103
	v_max_i32_e32 v103, 0, v103
	s_mov_b32 m0, s10
	v_mad_u64_u32 v[108:109], vcc, v103, s16, v[106:107]
	global_load_lds_dwordx4 v[108:109], off
	v_add_u32_e32 v102, 8, v102
	v_mul_lo_u32 v103, v102, s81
	v_add_u32_e32 v103, s82, v103
	v_max_i32_e32 v103, 0, v103
	s_add_u32 m0, s10, 0x400
	v_mad_u64_u32 v[108:109], vcc, v103, s16, v[106:107]
	global_load_lds_dwordx4 v[108:109], off
	v_add_u32_e32 v102, 8, v102
	v_mul_lo_u32 v103, v102, s81
	v_add_u32_e32 v103, s82, v103
	v_max_i32_e32 v103, 0, v103
	s_add_u32 m0, s10, 0x800
	v_mad_u64_u32 v[108:109], vcc, v103, s16, v[106:107]
	global_load_lds_dwordx4 v[108:109], off
	v_add_u32_e32 v102, 8, v102
	v_mul_lo_u32 v103, v102, s81
	v_add_u32_e32 v103, s82, v103
	v_max_i32_e32 v103, 0, v103
	s_add_u32 m0, s10, 0xc00
	v_mad_u64_u32 v[108:109], vcc, v103, s16, v[106:107]
	global_load_lds_dwordx4 v[108:109], off
	s_add_u32 s13, s11, 4
	s_cmp_eq_u32 s11, 0
	s_cselect_b32 s13, 0, s13
	s_lshl_b32 s10, s13, 5
	v_add_u32_e32 v102, s10, v101
	s_lshl_b32 s10, s13, 12
	s_add_u32 s10, s10, s12
	v_mul_lo_u32 v103, v102, s81
	v_add_u32_e32 v103, s82, v103
	v_max_i32_e32 v103, 0, v103
	s_mov_b32 m0, s10
	v_mad_u64_u32 v[108:109], vcc, v103, s16, v[106:107]
	global_load_lds_dwordx4 v[108:109], off
	v_add_u32_e32 v102, 8, v102
	v_mul_lo_u32 v103, v102, s81
	v_add_u32_e32 v103, s82, v103
	v_max_i32_e32 v103, 0, v103
	s_add_u32 m0, s10, 0x400
	v_mad_u64_u32 v[108:109], vcc, v103, s16, v[106:107]
	global_load_lds_dwordx4 v[108:109], off
	v_add_u32_e32 v102, 8, v102
	v_mul_lo_u32 v103, v102, s81
	v_add_u32_e32 v103, s82, v103
	v_max_i32_e32 v103, 0, v103
	s_add_u32 m0, s10, 0x800
	v_mad_u64_u32 v[108:109], vcc, v103, s16, v[106:107]
	global_load_lds_dwordx4 v[108:109], off
	v_add_u32_e32 v102, 8, v102
	v_mul_lo_u32 v103, v102, s81
	v_add_u32_e32 v103, s82, v103
	v_max_i32_e32 v103, 0, v103
	s_add_u32 m0, s10, 0xc00
	v_mad_u64_u32 v[108:109], vcc, v103, s16, v[106:107]
	global_load_lds_dwordx4 v[108:109], off
	v_and_b32_e32 v100, 63, v0
	v_lshrrev_b32_e32 v101, 3, v100
	v_and_b32_e32 v104, 7, v100
	v_lshlrev_b32_e32 v104, 4, v104
	s_lshl_b32 s10, s88, 7
	s_add_u32 s10, s10, 0x1000
	v_add_u32_e32 v104, s10, v104
	v_mov_b32_e32 v105, 0
	v_lshl_add_u64 v[106:107], s[84:85], 0, v[104:105]
	s_bfe_u32 s11, s75, 0x2000c
	s_and_b32 s12, s75, 0xffff0000
	s_add_u32 s13, s11, 1
	s_lshl_b32 s10, s13, 5
	v_add_u32_e32 v102, s10, v101
	s_lshl_b32 s10, s13, 12
	s_add_u32 s10, s10, s12
	v_mul_lo_u32 v103, v102, s81
	v_add_u32_e32 v103, s82, v103
	v_max_i32_e32 v103, 0, v103
	s_mov_b32 m0, s10
	v_mad_u64_u32 v[108:109], vcc, v103, s16, v[106:107]
	global_load_lds_dwordx4 v[108:109], off
	v_add_u32_e32 v102, 8, v102
	v_mul_lo_u32 v103, v102, s81
	v_add_u32_e32 v103, s82, v103
	v_max_i32_e32 v103, 0, v103
	s_add_u32 m0, s10, 0x400
	v_mad_u64_u32 v[108:109], vcc, v103, s16, v[106:107]
	global_load_lds_dwordx4 v[108:109], off
	v_add_u32_e32 v102, 8, v102
	v_mul_lo_u32 v103, v102, s81
	v_add_u32_e32 v103, s82, v103
	v_max_i32_e32 v103, 0, v103
	s_add_u32 m0, s10, 0x800
	v_mad_u64_u32 v[108:109], vcc, v103, s16, v[106:107]
	global_load_lds_dwordx4 v[108:109], off
	v_add_u32_e32 v102, 8, v102
	v_mul_lo_u32 v103, v102, s81
	v_add_u32_e32 v103, s82, v103
	v_max_i32_e32 v103, 0, v103
	s_add_u32 m0, s10, 0xc00
	v_mad_u64_u32 v[108:109], vcc, v103, s16, v[106:107]
	global_load_lds_dwordx4 v[108:109], off
	s_add_u32 s13, s11, 4
	s_cmp_eq_u32 s11, 0
	s_cselect_b32 s13, 0, s13
	s_lshl_b32 s10, s13, 5
	v_add_u32_e32 v102, s10, v101
	s_lshl_b32 s10, s13, 12
	s_add_u32 s10, s10, s12
	v_mul_lo_u32 v103, v102, s81
	v_add_u32_e32 v103, s82, v103
	v_max_i32_e32 v103, 0, v103
	s_mov_b32 m0, s10
	v_mad_u64_u32 v[108:109], vcc, v103, s16, v[106:107]
	global_load_lds_dwordx4 v[108:109], off
	v_add_u32_e32 v102, 8, v102
	v_mul_lo_u32 v103, v102, s81
	v_add_u32_e32 v103, s82, v103
	v_max_i32_e32 v103, 0, v103
	s_add_u32 m0, s10, 0x400
	v_mad_u64_u32 v[108:109], vcc, v103, s16, v[106:107]
	global_load_lds_dwordx4 v[108:109], off
	v_add_u32_e32 v102, 8, v102
	v_mul_lo_u32 v103, v102, s81
	v_add_u32_e32 v103, s82, v103
	v_max_i32_e32 v103, 0, v103
	s_add_u32 m0, s10, 0x800
	v_mad_u64_u32 v[108:109], vcc, v103, s16, v[106:107]
	global_load_lds_dwordx4 v[108:109], off
	v_add_u32_e32 v102, 8, v102
	v_mul_lo_u32 v103, v102, s81
	v_add_u32_e32 v103, s82, v103
	v_max_i32_e32 v103, 0, v103
	s_add_u32 m0, s10, 0xc00
	v_mad_u64_u32 v[108:109], vcc, v103, s16, v[106:107]
	global_load_lds_dwordx4 v[108:109], off
	s_waitcnt vmcnt(0)
	s_barrier
	s_andn2_b64 vcc, exec, s[8:9]
	s_cbranch_vccz .LBB0_429
	s_branch .LBB0_492

.LBB0_431:
	ds_read_b128 v[2:5], v221 offset:32768
	s_cmp_lt_i32 s33, 1
	s_cselect_b64 s[78:79], -1, 0
	s_lshl_b32 s37, s88, 6
	s_waitcnt lgkmcnt(0)
	v_mfma_f32_32x32x16_bf16 v[18:33], v[2:5], v[158:161], 0
	ds_read_b128 v[2:5], v222 offset:32768
	s_waitcnt lgkmcnt(0)
	v_mfma_f32_32x32x16_bf16 v[18:33], v[2:5], v[154:157], v[18:33]
	ds_read_b128 v[2:5], v223 offset:32768
	s_waitcnt lgkmcnt(0)
	v_mfma_f32_32x32x16_bf16 v[18:33], v[2:5], v[150:153], v[18:33]
	ds_read_b128 v[2:5], v224 offset:32768
	s_waitcnt lgkmcnt(0)
	s_waitcnt lgkmcnt(0)
	v_mfma_f32_32x32x16_bf16 v[18:33], v[2:5], v[146:149], v[18:33]
	s_mov_b64 s[4:5], -1
	s_and_b64 vcc, exec, s[78:79]
	s_cbranch_vccz .LBB0_433
	v_mov_b32_e32 v2, v0
	s_lshl_b32 s90, s37, 1
	v_lshrrev_b32_e32 v3, 3, v2
	v_bfe_u32 v8, v2, 3, 3
	v_xor_b32_e32 v6, v3, v2
	v_or_b32_e32 v2, s2, v8
	v_mul_lo_u32 v2, v2, s81
	v_add_u32_e32 v2, s82, v2
	v_max_i32_e32 v4, 0, v2
	v_mov_b64_e32 v[2:3], s[84:85]
	v_mad_u64_u32 v[4:5], s[4:5], v4, s21, v[2:3]
	v_lshlrev_b32_e32 v6, 4, v6
	v_lshl_add_u64 v[4:5], v[4:5], 0, s[90:91]
	v_and_b32_e32 v6, 0x70, v6
	v_mov_b32_e32 v7, v179
	v_lshl_add_u64 v[4:5], v[4:5], 0, v[6:7]
	s_mov_b32 m0, s22
	v_lshl_add_u64 v[4:5], v[4:5], 0, s[92:93]
	v_or_b32_e32 v4, s10, v8
	v_mul_lo_u32 v4, v4, s81
	v_add_u32_e32 v4, s82, v4
	v_max_i32_e32 v4, 0, v4
	v_mad_u64_u32 v[4:5], s[4:5], v4, s21, v[2:3]
	v_lshl_add_u64 v[4:5], v[4:5], 0, s[90:91]
	v_lshl_add_u64 v[4:5], v[4:5], 0, v[6:7]
	v_lshl_add_u64 v[4:5], v[4:5], 0, s[92:93]
	s_mov_b32 m0, s23
	s_nop 0
	v_or_b32_e32 v4, s11, v8
	v_mul_lo_u32 v4, v4, s81
	v_add_u32_e32 v4, s82, v4
	v_max_i32_e32 v4, 0, v4
	v_mad_u64_u32 v[4:5], s[4:5], v4, s21, v[2:3]
	v_lshl_add_u64 v[4:5], v[4:5], 0, s[90:91]
	v_lshl_add_u64 v[4:5], v[4:5], 0, v[6:7]
	v_lshl_add_u64 v[4:5], v[4:5], 0, s[92:93]
	s_mov_b32 m0, s24
	s_nop 0
	v_or_b32_e32 v4, s12, v8
	v_mul_lo_u32 v4, v4, s81
	v_add_u32_e32 v4, s82, v4
	v_max_i32_e32 v4, 0, v4
	v_mad_u64_u32 v[2:3], s[4:5], v4, s21, v[2:3]
	v_lshl_add_u64 v[2:3], v[2:3], 0, s[90:91]
	v_lshl_add_u64 v[2:3], v[2:3], 0, v[6:7]
	v_lshl_add_u64 v[2:3], v[2:3], 0, s[92:93]
	s_mov_b64 s[4:5], 0
.LBB0_433:
	v_lshl_add_u64 v[50:51], s[84:85], 0, v[178:179]
	s_andn2_b64 vcc, exec, s[4:5]
	s_mul_i32 s89, s81, 0x48
	s_mul_i32 s87, s81, 0x50
	s_mul_i32 s43, s81, 0x58
	s_cbranch_vccnz .LBB0_435
	s_lshl_b32 s4, s81, 6
	s_mov_b32 m0, s22
	v_mad_i64_i32 v[2:3], s[4:5], s4, v225, v[50:51]
	v_mad_i64_i32 v[2:3], s[4:5], s89, v225, v[50:51]
	s_mov_b32 m0, s23
	s_nop 0
	v_mad_i64_i32 v[2:3], s[4:5], s87, v225, v[50:51]
	s_mov_b32 m0, s24
	s_nop 0
	v_mad_i64_i32 v[2:3], s[4:5], s43, v225, v[50:51]
.LBB0_435:
	s_mov_b32 m0, s25
	s_mov_b64 s[4:5], -1
	s_and_b64 vcc, exec, s[78:79]
	s_cbranch_vccz .LBB0_437
	v_mov_b32_e32 v6, v0
	s_lshl_b32 s90, s37, 1
	v_bfe_u32 v8, v6, 3, 3
	v_or_b32_e32 v2, s3, v8
	v_mul_lo_u32 v2, v2, s81
	v_add_u32_e32 v2, s82, v2
	v_max_i32_e32 v4, 0, v2
	v_mov_b64_e32 v[2:3], s[84:85]
	v_mad_u64_u32 v[4:5], s[4:5], v4, s21, v[2:3]
	v_lshlrev_b32_e32 v6, 4, v6
	v_lshl_add_u64 v[4:5], v[4:5], 0, s[90:91]
	v_and_b32_e32 v6, 0x70, v6
	v_mov_b32_e32 v7, v179
	v_lshl_add_u64 v[4:5], v[4:5], 0, v[6:7]
	s_mov_b32 m0, s75
	v_lshl_add_u64 v[4:5], v[4:5], 0, s[94:95]
	v_readlane_b32 s4, v254, 24
	s_nop 0
	v_or_b32_e32 v4, s4, v8
	v_mul_lo_u32 v4, v4, s81
	v_add_u32_e32 v4, s82, v4
	v_max_i32_e32 v4, 0, v4
	v_mad_u64_u32 v[4:5], s[4:5], v4, s21, v[2:3]
	v_lshl_add_u64 v[4:5], v[4:5], 0, s[90:91]
	v_lshl_add_u64 v[4:5], v[4:5], 0, v[6:7]
	v_lshl_add_u64 v[4:5], v[4:5], 0, s[94:95]
	s_mov_b32 m0, s26
	v_readlane_b32 s4, v254, 25
	s_nop 0
	v_or_b32_e32 v4, s4, v8
	v_mul_lo_u32 v4, v4, s81
	v_add_u32_e32 v4, s82, v4
	v_max_i32_e32 v4, 0, v4
	v_mad_u64_u32 v[4:5], s[4:5], v4, s21, v[2:3]
	v_lshl_add_u64 v[4:5], v[4:5], 0, s[90:91]
	v_lshl_add_u64 v[4:5], v[4:5], 0, v[6:7]
	v_lshl_add_u64 v[4:5], v[4:5], 0, s[94:95]
	s_add_i32 m0, s75, 0x800
	v_readlane_b32 s4, v254, 26
	s_nop 0
	v_or_b32_e32 v4, s4, v8
	v_mul_lo_u32 v4, v4, s81
	v_add_u32_e32 v4, s82, v4
	v_max_i32_e32 v4, 0, v4
	v_mad_u64_u32 v[2:3], s[4:5], v4, s21, v[2:3]
	v_lshl_add_u64 v[2:3], v[2:3], 0, s[90:91]
	v_lshl_add_u64 v[2:3], v[2:3], 0, v[6:7]
	v_lshl_add_u64 v[2:3], v[2:3], 0, s[94:95]
	s_mov_b64 s[4:5], 0
.LBB0_437:
	v_mov_b32_e32 v183, v179
	s_andn2_b64 vcc, exec, s[4:5]
	v_lshl_add_u64 v[188:189], s[84:85], 0, v[182:183]
	s_cbranch_vccnz .LBB0_439
	s_lshl_b32 s4, s81, 3
	s_mov_b32 m0, s75
	v_mad_i64_i32 v[2:3], s[4:5], s4, v225, v[188:189]
	s_mov_b32 m0, s26
	s_lshl_b32 s4, s81, 4
	v_mad_i64_i32 v[2:3], s[4:5], s4, v225, v[188:189]
	s_add_i32 m0, s75, 0x800
	s_mul_i32 s4, s81, 24
	v_mad_i64_i32 v[2:3], s[4:5], s4, v225, v[188:189]
.LBB0_439:
	s_mov_b32 m0, s27
	s_mov_b64 s[4:5], -1
	s_and_b64 vcc, exec, s[78:79]
	s_cbranch_vccz .LBB0_441
	v_mov_b32_e32 v6, v0
	v_readlane_b32 s4, v254, 21
	v_bfe_u32 v8, v6, 3, 3
	s_lshl_b32 s90, s37, 1
	v_or_b32_e32 v2, s4, v8
	v_mul_lo_u32 v2, v2, s81
	v_add_u32_e32 v2, s82, v2
	v_max_i32_e32 v4, 0, v2
	v_mov_b64_e32 v[2:3], s[84:85]
	v_mad_u64_u32 v[4:5], s[4:5], v4, s21, v[2:3]
	v_lshlrev_b32_e32 v6, 4, v6
	v_lshl_add_u64 v[4:5], v[4:5], 0, s[90:91]
	v_and_b32_e32 v6, 0x70, v6
	v_mov_b32_e32 v7, v179
	v_lshl_add_u64 v[4:5], v[4:5], 0, v[6:7]
	s_mov_b32 m0, s83
	v_lshl_add_u64 v[4:5], v[4:5], 0, s[94:95]
	v_readlane_b32 s4, v254, 27
	s_nop 0
	v_or_b32_e32 v4, s4, v8
	v_mul_lo_u32 v4, v4, s81
	v_add_u32_e32 v4, s82, v4
	v_max_i32_e32 v4, 0, v4
	v_mad_u64_u32 v[4:5], s[4:5], v4, s21, v[2:3]
	v_lshl_add_u64 v[4:5], v[4:5], 0, s[90:91]
	v_lshl_add_u64 v[4:5], v[4:5], 0, v[6:7]
	v_lshl_add_u64 v[4:5], v[4:5], 0, s[94:95]
	s_mov_b32 m0, s28
	v_readlane_b32 s4, v254, 28
	s_nop 0
	v_or_b32_e32 v4, s4, v8
	v_mul_lo_u32 v4, v4, s81
	v_add_u32_e32 v4, s82, v4
	v_max_i32_e32 v4, 0, v4
	v_mad_u64_u32 v[4:5], s[4:5], v4, s21, v[2:3]
	v_lshl_add_u64 v[4:5], v[4:5], 0, s[90:91]
	v_lshl_add_u64 v[4:5], v[4:5], 0, v[6:7]
	v_lshl_add_u64 v[4:5], v[4:5], 0, s[94:95]
	s_mov_b32 m0, s29
	v_readlane_b32 s4, v254, 29
	s_nop 0
	v_or_b32_e32 v4, s4, v8
	v_mul_lo_u32 v4, v4, s81
	v_add_u32_e32 v4, s82, v4
	v_max_i32_e32 v4, 0, v4
	v_mad_u64_u32 v[2:3], s[4:5], v4, s21, v[2:3]
	v_lshl_add_u64 v[2:3], v[2:3], 0, s[90:91]
	v_lshl_add_u64 v[2:3], v[2:3], 0, v[6:7]
	v_lshl_add_u64 v[2:3], v[2:3], 0, s[94:95]
	s_mov_b64 s[4:5], 0
.LBB0_441:
	s_andn2_b64 vcc, exec, s[4:5]
	s_cbranch_vccnz .LBB0_443
	s_lshl_b32 s4, s81, 5
	v_mad_i64_i32 v[2:3], s[4:5], s4, v225, v[188:189]
	s_mov_b32 m0, s83
	s_mul_i32 s4, s81, 40
	v_mad_i64_i32 v[2:3], s[4:5], s4, v225, v[188:189]
	s_mov_b32 m0, s28
	s_mul_i32 s4, s81, 48
	v_mad_i64_i32 v[2:3], s[4:5], s4, v225, v[188:189]
	s_mov_b32 m0, s29
	s_mul_i32 s4, s81, 56
	v_mad_i64_i32 v[2:3], s[4:5], s4, v225, v[188:189]
.LBB0_443:
	s_mov_b32 m0, s30
	ds_read_b128 v[34:37], v222 offset:36864
	ds_read_b128 v[2:5], v221 offset:36864
	s_waitcnt lgkmcnt(0)
	v_mfma_f32_32x32x16_bf16 v[2:17], v[2:5], v[158:161], 0
	v_mfma_f32_32x32x16_bf16 v[2:17], v[34:37], v[154:157], v[2:17]
	ds_read_b128 v[34:37], v223 offset:36864
	s_waitcnt lgkmcnt(0)
	v_mfma_f32_32x32x16_bf16 v[2:17], v[34:37], v[150:153], v[2:17]
	ds_read_b128 v[34:37], v224 offset:36864
	s_waitcnt lgkmcnt(0)
	s_waitcnt lgkmcnt(0)
	v_mfma_f32_32x32x16_bf16 v[2:17], v[34:37], v[146:149], v[2:17]
	v_cndmask_b32_e64 v34, 0, 1, s[78:79]
	v_cmp_ne_u32_e64 s[72:73], 1, v34
	s_andn2_b64 vcc, exec, s[78:79]
	s_mov_b64 s[4:5], -1
	s_cbranch_vccnz .LBB0_445
	v_mov_b32_e32 v34, v0
	s_lshl_b32 s90, s37, 1
	v_lshrrev_b32_e32 v35, 3, v34
	v_bfe_u32 v40, v34, 3, 3
	v_xor_b32_e32 v38, v35, v34
	v_or_b32_e32 v34, s13, v40
	v_mul_lo_u32 v34, v34, s81
	v_add_u32_e32 v34, s82, v34
	v_max_i32_e32 v36, 0, v34
	v_mov_b64_e32 v[34:35], s[84:85]
	v_mad_u64_u32 v[36:37], s[4:5], v36, s21, v[34:35]
	v_lshlrev_b32_e32 v38, 4, v38
	v_lshl_add_u64 v[36:37], v[36:37], 0, s[90:91]
	v_and_b32_e32 v38, 0x70, v38
	v_mov_b32_e32 v39, v179
	v_lshl_add_u64 v[36:37], v[36:37], 0, v[38:39]
	s_mov_b32 m0, s31
	v_lshl_add_u64 v[36:37], v[36:37], 0, s[92:93]
	v_or_b32_e32 v36, s14, v40
	v_mul_lo_u32 v36, v36, s81
	v_add_u32_e32 v36, s82, v36
	v_max_i32_e32 v36, 0, v36
	v_mad_u64_u32 v[36:37], s[4:5], v36, s21, v[34:35]
	v_lshl_add_u64 v[36:37], v[36:37], 0, s[90:91]
	v_lshl_add_u64 v[36:37], v[36:37], 0, v[38:39]
	v_lshl_add_u64 v[36:37], v[36:37], 0, s[92:93]
	s_mov_b32 m0, s34
	s_nop 0
	v_or_b32_e32 v36, s15, v40
	v_mul_lo_u32 v36, v36, s81
	v_add_u32_e32 v36, s82, v36
	v_max_i32_e32 v36, 0, v36
	v_mad_u64_u32 v[36:37], s[4:5], v36, s21, v[34:35]
	v_lshl_add_u64 v[36:37], v[36:37], 0, s[90:91]
	v_lshl_add_u64 v[36:37], v[36:37], 0, v[38:39]
	v_lshl_add_u64 v[36:37], v[36:37], 0, s[92:93]
	s_mov_b32 m0, s35
	s_nop 0
	v_or_b32_e32 v36, s16, v40
	v_mul_lo_u32 v36, v36, s81
	v_add_u32_e32 v36, s82, v36
	v_max_i32_e32 v36, 0, v36
	v_mad_u64_u32 v[34:35], s[4:5], v36, s21, v[34:35]
	v_lshl_add_u64 v[34:35], v[34:35], 0, s[90:91]
	v_lshl_add_u64 v[34:35], v[34:35], 0, v[38:39]
	v_lshl_add_u64 v[34:35], v[34:35], 0, s[92:93]
	s_mov_b64 s[4:5], 0
.LBB0_445:
	s_andn2_b64 vcc, exec, s[4:5]
	s_mul_i32 s52, s81, 0x60
	s_mul_i32 s51, s81, 0x68
	s_mul_i32 s50, s81, 0x70
	s_mul_i32 s49, s81, 0x78
	s_cbranch_vccnz .LBB0_447
	s_mov_b32 m0, s31
	v_mad_i64_i32 v[34:35], s[4:5], s52, v225, v[50:51]
	v_mad_i64_i32 v[34:35], s[4:5], s51, v225, v[50:51]
	s_mov_b32 m0, s34
	s_nop 0
	v_mad_i64_i32 v[34:35], s[4:5], s50, v225, v[50:51]
	s_mov_b32 m0, s35
	s_nop 0
	v_mad_i64_i32 v[34:35], s[4:5], s49, v225, v[50:51]
.LBB0_447:
	s_mov_b32 m0, s36
	s_nop 0
	ds_read_b128 v[34:37], v221 offset:40960
	ds_read_b128 v[52:55], v222 offset:40960
	s_waitcnt lgkmcnt(0)
	v_mfma_f32_32x32x16_bf16 v[34:49], v[34:37], v[158:161], 0
	v_mfma_f32_32x32x16_bf16 v[34:49], v[52:55], v[154:157], v[34:49]
	ds_read_b128 v[52:55], v223 offset:40960
	s_waitcnt lgkmcnt(0)
	v_mfma_f32_32x32x16_bf16 v[34:49], v[52:55], v[150:153], v[34:49]
	ds_read_b128 v[52:55], v224 offset:40960
	s_waitcnt lgkmcnt(0)
	s_waitcnt lgkmcnt(0)
	v_mfma_f32_32x32x16_bf16 v[34:49], v[52:55], v[146:149], v[34:49]
	s_and_b64 vcc, exec, s[72:73]
	s_mov_b64 s[4:5], -1
	s_cbranch_vccnz .LBB0_449
	v_mov_b32_e32 v52, v0
	s_lshl_b32 s90, s37, 1
	v_lshrrev_b32_e32 v53, 3, v52
	v_bfe_u32 v58, v52, 3, 3
	v_xor_b32_e32 v56, v53, v52
	v_or_b32_e32 v52, s17, v58
	v_mul_lo_u32 v52, v52, s81
	v_add_u32_e32 v52, s82, v52
	v_max_i32_e32 v54, 0, v52
	v_mov_b64_e32 v[52:53], s[84:85]
	v_mad_u64_u32 v[54:55], s[4:5], v54, s21, v[52:53]
	v_lshlrev_b32_e32 v56, 4, v56
	v_lshl_add_u64 v[54:55], v[54:55], 0, s[90:91]
	v_and_b32_e32 v56, 0x70, v56
	v_mov_b32_e32 v57, v179
	v_lshl_add_u64 v[54:55], v[54:55], 0, v[56:57]
	s_mov_b32 m0, s22
	v_lshl_add_u64 v[54:55], v[54:55], 0, s[92:93]
	v_or_b32_e32 v54, s18, v58
	v_mul_lo_u32 v54, v54, s81
	v_add_u32_e32 v54, s82, v54
	v_max_i32_e32 v54, 0, v54
	v_mad_u64_u32 v[54:55], s[4:5], v54, s21, v[52:53]
	v_lshl_add_u64 v[54:55], v[54:55], 0, s[90:91]
	v_lshl_add_u64 v[54:55], v[54:55], 0, v[56:57]
	v_lshl_add_u64 v[54:55], v[54:55], 0, s[92:93]
	s_mov_b32 m0, s23
	s_nop 0
	v_or_b32_e32 v54, s19, v58
	v_mul_lo_u32 v54, v54, s81
	v_add_u32_e32 v54, s82, v54
	v_max_i32_e32 v54, 0, v54
	v_mad_u64_u32 v[54:55], s[4:5], v54, s21, v[52:53]
	v_lshl_add_u64 v[54:55], v[54:55], 0, s[90:91]
	v_lshl_add_u64 v[54:55], v[54:55], 0, v[56:57]
	v_lshl_add_u64 v[54:55], v[54:55], 0, s[92:93]
	s_mov_b32 m0, s24
	s_nop 0
	v_or_b32_e32 v54, s20, v58
	v_mul_lo_u32 v54, v54, s81
	v_add_u32_e32 v54, s82, v54
	v_max_i32_e32 v54, 0, v54
	v_mad_u64_u32 v[52:53], s[4:5], v54, s21, v[52:53]
	v_lshl_add_u64 v[52:53], v[52:53], 0, s[90:91]
	v_lshl_add_u64 v[52:53], v[52:53], 0, v[56:57]
	v_lshl_add_u64 v[52:53], v[52:53], 0, s[92:93]
	s_mov_b64 s[4:5], 0
.LBB0_449:
	s_andn2_b64 vcc, exec, s[4:5]
	s_mul_i32 s46, s81, 0x88
	s_mul_i32 s45, s81, 0x90
	s_mul_i32 s44, s81, 0x98
	s_cbranch_vccnz .LBB0_451
	s_lshl_b32 s4, s81, 7
	s_mov_b32 m0, s22
	v_mad_i64_i32 v[52:53], s[4:5], s4, v225, v[50:51]
	v_mad_i64_i32 v[52:53], s[4:5], s46, v225, v[50:51]
	s_mov_b32 m0, s23
	s_nop 0
	v_mad_i64_i32 v[52:53], s[4:5], s45, v225, v[50:51]
	s_mov_b32 m0, s24
	s_nop 0
	v_mad_i64_i32 v[52:53], s[4:5], s44, v225, v[50:51]
.LBB0_451:
	s_mov_b32 m0, s25
	s_nop 0
	ds_read_b128 v[50:53], v221 offset:45056
	ds_read_b128 v[66:69], v222 offset:45056
	s_waitcnt lgkmcnt(0)
	v_mfma_f32_32x32x16_bf16 v[50:65], v[50:53], v[158:161], 0
	v_mfma_f32_32x32x16_bf16 v[50:65], v[66:69], v[154:157], v[50:65]
	ds_read_b128 v[66:69], v223 offset:45056
	s_waitcnt lgkmcnt(0)
	v_mfma_f32_32x32x16_bf16 v[50:65], v[66:69], v[150:153], v[50:65]
	ds_read_b128 v[66:69], v224 offset:45056
	s_waitcnt lgkmcnt(0)
	s_waitcnt lgkmcnt(0)
	v_mfma_f32_32x32x16_bf16 v[50:65], v[66:69], v[146:149], v[50:65]
	ds_read_b128 v[66:69], v221 offset:49152
	ds_read_b128 v[82:85], v222 offset:49152
	s_waitcnt lgkmcnt(0)
	v_mfma_f32_32x32x16_bf16 v[66:81], v[66:69], v[158:161], 0
	v_mfma_f32_32x32x16_bf16 v[66:81], v[82:85], v[154:157], v[66:81]
	ds_read_b128 v[82:85], v223 offset:49152
	s_waitcnt lgkmcnt(0)
	v_mfma_f32_32x32x16_bf16 v[66:81], v[82:85], v[150:153], v[66:81]
	ds_read_b128 v[82:85], v224 offset:49152
	s_waitcnt lgkmcnt(0)
	s_waitcnt lgkmcnt(0)
	v_mfma_f32_32x32x16_bf16 v[66:81], v[82:85], v[146:149], v[66:81]
	s_waitcnt vmcnt(0)
	s_barrier
	s_add_i32 s38, s53, 1
	s_cmp_lt_i32 s38, s0
	s_cselect_b64 s[96:97], -1, 0
	s_cmp_ge_i32 s38, s0
	s_mov_b32 s39, s86
	s_mov_b32 s40, s88
	s_mov_b32 s47, s81
	s_mov_b32 s41, s33
	s_mov_b32 s80, s42
	s_mov_b32 s48, s82
	v_mov_b32_e32 v183, v180
	v_mov_b32_e32 v190, v178
	v_mov_b32_e32 v187, v182
	s_cbranch_scc1 .LBB0_466
	v_readlane_b32 s40, v254, 8
	v_readlane_b32 s41, v254, 9
	s_mov_b64 s[4:5], -1
	s_and_b64 vcc, exec, s[40:41]
	s_cbranch_vccz .LBB0_454
	s_mul_i32 s4, s38, s74
	v_readlane_b32 s40, v254, 19
	v_readlane_b32 s41, v254, 20
	s_add_i32 s39, s4, s40
	s_mov_b64 s[4:5], 0

.LBB0_459:
	s_lshl_b32 s4, s39, 1
	v_readlane_b32 s5, v254, 14
	s_add_i32 s4, s4, s5
	s_ashr_i32 s39, s4, 11
	s_bfe_u32 s5, s4, 0x70004
	s_lshl_b32 s48, s39, 1
	s_and_b32 s40, s4, 15
	s_lshr_b32 s41, s5, s48
	s_bfm_b32 s4, s48, 0
	s_and_b32 s4, s4, s5
	s_lshl_b32 s5, s41, 7
	s_lshl_b32 s5, s5, s48
	s_or_b32 s80, s5, s4
	v_lshlrev_b32_e32 v82, s48, v192
	v_add_u32_e32 v82, s80, v82
	s_movk_i32 s4, 0xc40
	v_mul_lo_u32 v82, v82, s4
	s_lshl_b32 s47, s40, 6
	v_add_lshl_u32 v84, v82, s47, 1
	s_cmp_lg_u32 s41, 0
	s_cselect_b64 s[4:5], -1, 0
	s_cmp_eq_u32 s41, 0
	v_add_u32_e32 v190, v207, v84
	s_cbranch_scc1 .LBB0_489
	v_mov_b32_e32 v191, v179
	s_mov_b32 m0, s22
	v_lshl_add_u64 v[82:83], s[84:85], 0, v[190:191]
	s_lshl_b32 s53, 8, s48
	v_mad_i64_i32 v[86:87], vcc, s53, v225, v[82:83]
	s_mov_b32 m0, s23
	s_lshl_b32 s53, 16, s48
	v_mad_u64_u32 v[86:87], vcc, s53, v225, v[82:83]
	s_mov_b32 m0, s24
	s_lshl_b32 s53, 24, s48
	v_mad_i64_i32 v[82:83], vcc, s53, v225, v[82:83]
	s_cbranch_execnz .LBB0_462
.LBB0_461:
	v_mov_b32_e32 v82, v0
	v_readlane_b32 s53, v254, 22
	v_lshrrev_b32_e32 v83, 3, v82
	v_bfe_u32 v85, v82, 3, 3
	v_xor_b32_e32 v88, v83, v82
	v_or_b32_e32 v82, s53, v85
	v_lshlrev_b32_e32 v82, s48, v82
	v_add_u32_e32 v82, s80, v82
	v_max_i32_e32 v86, 0, v82
	v_mov_b64_e32 v[82:83], s[84:85]
	v_mad_u64_u32 v[86:87], vcc, v86, s21, v[82:83]
	s_lshl_b32 s90, s47, 1
	v_lshlrev_b32_e32 v88, 4, v88
	v_lshl_add_u64 v[86:87], v[86:87], 0, s[90:91]
	v_and_b32_e32 v88, 0x70, v88
	v_mov_b32_e32 v89, v179
	v_lshl_add_u64 v[86:87], v[86:87], 0, v[88:89]
	s_mov_b32 m0, s22
	v_lshl_add_u64 v[86:87], v[86:87], 0, s[92:93]
	v_readlane_b32 s53, v254, 30
	s_nop 0
	v_or_b32_e32 v86, s53, v85
	v_lshlrev_b32_e32 v86, s48, v86
	v_add_u32_e32 v86, s80, v86
	v_max_i32_e32 v86, 0, v86
	v_mad_u64_u32 v[86:87], vcc, v86, s21, v[82:83]
	v_lshl_add_u64 v[86:87], v[86:87], 0, s[90:91]
	v_lshl_add_u64 v[86:87], v[86:87], 0, v[88:89]
	v_lshl_add_u64 v[86:87], v[86:87], 0, s[92:93]
	s_mov_b32 m0, s23
	v_readlane_b32 s53, v254, 31
	s_nop 0
	v_or_b32_e32 v86, s53, v85
	v_lshlrev_b32_e32 v86, s48, v86
	v_add_u32_e32 v86, s80, v86
	v_max_i32_e32 v86, 0, v86
	v_mad_u64_u32 v[86:87], vcc, v86, s21, v[82:83]
	v_lshl_add_u64 v[86:87], v[86:87], 0, s[90:91]
	v_lshl_add_u64 v[86:87], v[86:87], 0, v[88:89]
	v_lshl_add_u64 v[86:87], v[86:87], 0, s[92:93]
	s_mov_b32 m0, s24
	v_readlane_b32 s53, v254, 32
	s_nop 0
	v_or_b32_e32 v85, s53, v85
	v_lshlrev_b32_e32 v85, s48, v85
	v_add_u32_e32 v85, s80, v85
	v_max_i32_e32 v85, 0, v85
	v_mad_u64_u32 v[82:83], vcc, v85, s21, v[82:83]
	v_lshl_add_u64 v[82:83], v[82:83], 0, s[90:91]
	v_lshl_add_u64 v[82:83], v[82:83], 0, v[88:89]
	v_lshl_add_u64 v[82:83], v[82:83], 0, s[92:93]
.LBB0_462:
	s_mov_b32 m0, s25
	s_andn2_b64 vcc, exec, s[4:5]
	s_cbranch_vccnz .LBB0_490
	v_mov_b32_e32 v191, v179
	v_lshl_add_u64 v[82:83], s[84:85], 0, v[190:191]
	s_lshl_b32 s4, 32, s48
	v_mad_i64_i32 v[86:87], s[4:5], s4, v225, v[82:83]
	s_mov_b32 m0, s31
	s_lshl_b32 s4, 40, s48
	v_mad_i64_i32 v[86:87], s[4:5], s4, v225, v[82:83]
	s_mov_b32 m0, s34
	s_lshl_b32 s4, 48, s48
	v_mad_i64_i32 v[86:87], s[4:5], s4, v225, v[82:83]
	s_mov_b32 m0, s35
	s_lshl_b32 s4, 56, s48
	v_mad_i64_i32 v[82:83], s[4:5], s4, v225, v[82:83]
	s_mov_b32 m0, s36
	s_nop 0
	s_cbranch_execnz .LBB0_465
.LBB0_464:
	v_mov_b32_e32 v82, v0
	v_readlane_b32 s4, v254, 23
	v_lshrrev_b32_e32 v83, 3, v82
	v_bfe_u32 v85, v82, 3, 3
	v_xor_b32_e32 v88, v83, v82
	v_or_b32_e32 v82, s4, v85
	v_lshlrev_b32_e32 v82, s48, v82
	v_add_u32_e32 v82, s80, v82
	v_max_i32_e32 v86, 0, v82
	v_mov_b64_e32 v[82:83], s[84:85]
	v_mad_u64_u32 v[86:87], s[4:5], v86, s21, v[82:83]
	s_lshl_b32 s90, s47, 1
	v_lshlrev_b32_e32 v88, 4, v88
	v_lshl_add_u64 v[86:87], v[86:87], 0, s[90:91]
	v_and_b32_e32 v88, 0x70, v88
	v_mov_b32_e32 v89, v179
	v_lshl_add_u64 v[86:87], v[86:87], 0, v[88:89]
	s_mov_b32 m0, s31
	v_lshl_add_u64 v[86:87], v[86:87], 0, s[92:93]
	v_readlane_b32 s4, v254, 33
	s_nop 0
	v_or_b32_e32 v86, s4, v85
	v_lshlrev_b32_e32 v86, s48, v86
	v_add_u32_e32 v86, s80, v86
	v_max_i32_e32 v86, 0, v86
	v_mad_u64_u32 v[86:87], s[4:5], v86, s21, v[82:83]
	v_lshl_add_u64 v[86:87], v[86:87], 0, s[90:91]
	v_lshl_add_u64 v[86:87], v[86:87], 0, v[88:89]
	v_lshl_add_u64 v[86:87], v[86:87], 0, s[92:93]
	s_mov_b32 m0, s34
	v_readlane_b32 s4, v254, 34
	s_nop 0
	v_or_b32_e32 v86, s4, v85
	v_lshlrev_b32_e32 v86, s48, v86
	v_add_u32_e32 v86, s80, v86
	v_max_i32_e32 v86, 0, v86
	v_mad_u64_u32 v[86:87], s[4:5], v86, s21, v[82:83]
	v_readlane_b32 s4, v254, 35
	v_lshl_add_u64 v[86:87], v[86:87], 0, s[90:91]
	v_lshl_add_u64 v[86:87], v[86:87], 0, v[88:89]
	v_or_b32_e32 v85, s4, v85
	v_lshlrev_b32_e32 v85, s48, v85
	v_add_u32_e32 v85, s80, v85
	v_max_i32_e32 v85, 0, v85
	v_mad_u64_u32 v[82:83], s[4:5], v85, s21, v[82:83]
	v_lshl_add_u64 v[82:83], v[82:83], 0, s[90:91]
	v_lshl_add_u64 v[86:87], v[86:87], 0, s[92:93]
	s_mov_b32 m0, s35
	v_lshl_add_u64 v[82:83], v[82:83], 0, v[88:89]
	v_lshl_add_u64 v[82:83], v[82:83], 0, s[92:93]
	s_mov_b32 m0, s36
	s_nop 0
.LBB0_465:
	v_lshlrev_b32_e32 v82, s48, v1
	v_add_u32_e32 v183, s80, v82
	v_mov_b64_e32 v[82:83], s[84:85]
	v_mad_i64_i32 v[82:83], s[4:5], v183, s21, v[82:83]
	s_lshl_b32 s90, s47, 1
	v_lshl_add_u64 v[82:83], v[82:83], 0, s[90:91]
	v_mov_b32_e32 v187, v179
	v_lshl_add_u64 v[82:83], v[82:83], 0, v[186:187]
	global_load_dwordx4 v[162:165], v[82:83], off
	global_load_dwordx4 v[166:169], v[82:83], off offset:32
	global_load_dwordx4 v[170:173], v[82:83], off offset:64
	global_load_dwordx4 v[174:177], v[82:83], off offset:96
	s_lshl_b32 s4, 0xffffff80, s48
	s_lshl_b32 s47, 1, s48
	s_add_i32 s48, s80, s4
	v_add_u32_e32 v187, v208, v84
	v_and_b32_e32 v82, 63, v0
	v_lshrrev_b32_e32 v83, 3, v82
	v_and_b32_e32 v86, 7, v82
	v_xor_b32_e32 v86, v86, v83
	v_lshlrev_b32_e32 v86, 4, v86
	s_lshl_b32 s4, s40, 7
	s_add_u32 s4, s4, 0x800
	v_add_u32_e32 v86, s4, v86
	v_mov_b32_e32 v87, 0
	v_lshl_add_u64 v[88:89], s[84:85], 0, v[86:87]
	s_bfe_u32 s5, s75, 0x2000c
	s_and_b32 s53, s75, 0xffff0000
	s_add_u32 s53, s53, 0x8000
	s_add_u32 s90, s5, 1
	s_lshl_b32 s4, s90, 5
	v_add_u32_e32 v85, s4, v83
	s_lshl_b32 s4, s90, 12
	s_add_u32 s4, s4, s53
	v_mul_lo_u32 v92, v85, s47
	v_add_u32_e32 v92, s48, v92
	v_max_i32_e32 v92, 0, v92
	s_mov_b32 m0, s4
	v_mad_u64_u32 v[90:91], vcc, v92, s21, v[88:89]
	global_load_lds_dwordx4 v[90:91], off
	v_add_u32_e32 v85, 8, v85
	v_mul_lo_u32 v92, v85, s47
	v_add_u32_e32 v92, s48, v92
	v_max_i32_e32 v92, 0, v92
	s_add_u32 m0, s4, 0x400
	v_mad_u64_u32 v[90:91], vcc, v92, s21, v[88:89]
	global_load_lds_dwordx4 v[90:91], off
	v_add_u32_e32 v85, 8, v85
	v_mul_lo_u32 v92, v85, s47
	v_add_u32_e32 v92, s48, v92
	v_max_i32_e32 v92, 0, v92
	s_add_u32 m0, s4, 0x800
	v_mad_u64_u32 v[90:91], vcc, v92, s21, v[88:89]
	global_load_lds_dwordx4 v[90:91], off
	v_add_u32_e32 v85, 8, v85
	v_mul_lo_u32 v92, v85, s47
	v_add_u32_e32 v92, s48, v92
	v_max_i32_e32 v92, 0, v92
	s_add_u32 m0, s4, 0xc00
	v_mad_u64_u32 v[90:91], vcc, v92, s21, v[88:89]
	global_load_lds_dwordx4 v[90:91], off
	s_add_u32 s90, s5, 4
	s_cmp_eq_u32 s5, 0
	s_cselect_b32 s90, 0, s90
	s_lshl_b32 s4, s90, 5
	v_add_u32_e32 v85, s4, v83
	s_lshl_b32 s4, s90, 12
	s_add_u32 s4, s4, s53
	v_mul_lo_u32 v92, v85, s47
	v_add_u32_e32 v92, s48, v92
	v_max_i32_e32 v92, 0, v92
	s_mov_b32 m0, s4
	v_mad_u64_u32 v[90:91], vcc, v92, s21, v[88:89]
	global_load_lds_dwordx4 v[90:91], off
	v_add_u32_e32 v85, 8, v85
	v_mul_lo_u32 v92, v85, s47
	v_add_u32_e32 v92, s48, v92
	v_max_i32_e32 v92, 0, v92
	s_add_u32 m0, s4, 0x400
	v_mad_u64_u32 v[90:91], vcc, v92, s21, v[88:89]
	global_load_lds_dwordx4 v[90:91], off
	v_add_u32_e32 v85, 8, v85
	v_mul_lo_u32 v92, v85, s47
	v_add_u32_e32 v92, s48, v92
	v_max_i32_e32 v92, 0, v92
	s_add_u32 m0, s4, 0x800
	v_mad_u64_u32 v[90:91], vcc, v92, s21, v[88:89]
	global_load_lds_dwordx4 v[90:91], off
	v_add_u32_e32 v85, 8, v85
	v_mul_lo_u32 v92, v85, s47
	v_add_u32_e32 v92, s48, v92
	v_max_i32_e32 v92, 0, v92
	s_add_u32 m0, s4, 0xc00
	v_mad_u64_u32 v[90:91], vcc, v92, s21, v[88:89]
	global_load_lds_dwordx4 v[90:91], off

.LBB0_471:
	v_max_f32_e32 v33, v18, v18
	v_max_f32_e32 v66, v97, v97
	v_max_f32_e32 v33, v66, v33
	v_max_f32_e32 v66, v20, v20
	v_max_f32_e32 v67, v19, v19
	v_max_f32_e32 v66, v67, v66
	s_mov_b32 s4, 0xff800000
	v_max3_f32 v33, v33, s4, v66
	v_max_f32_e32 v66, v22, v22
	v_max_f32_e32 v67, v21, v21
	v_max_f32_e32 v66, v67, v66
	v_max_f32_e32 v67, v24, v24
	v_max_f32_e32 v68, v23, v23
	v_max_f32_e32 v67, v68, v67
	v_max3_f32 v33, v33, v66, v67
	v_max_f32_e32 v66, v26, v26
	v_max_f32_e32 v67, v25, v25
	v_max_f32_e32 v66, v67, v66
	v_max_f32_e32 v67, v28, v28
	v_max_f32_e32 v68, v27, v27
	v_max_f32_e32 v67, v68, v67
	v_max3_f32 v33, v33, v66, v67
	v_max_f32_e32 v66, v31, v31
	v_max_f32_e32 v67, v29, v29
	v_max_f32_e32 v66, v67, v66
	v_max_f32_e32 v67, v30, v30
	v_max_f32_e32 v68, v32, v32
	v_max_f32_e32 v67, v68, v67
	v_max3_f32 v33, v33, v66, v67
	v_max_f32_e32 v66, v3, v3
	v_max_f32_e32 v67, v2, v2
	v_max_f32_e32 v66, v67, v66
	v_max_f32_e32 v67, v5, v5
	v_max_f32_e32 v68, v4, v4
	v_max_f32_e32 v67, v68, v67
	v_max3_f32 v33, v33, v66, v67
	v_max_f32_e32 v66, v7, v7
	v_max_f32_e32 v67, v6, v6
	v_max_f32_e32 v66, v67, v66
	v_max_f32_e32 v67, v9, v9
	v_max_f32_e32 v68, v8, v8
	v_max_f32_e32 v67, v68, v67
	v_max3_f32 v33, v33, v66, v67
	v_max_f32_e32 v66, v11, v11
	v_max_f32_e32 v67, v10, v10
	v_max_f32_e32 v66, v67, v66
	v_max_f32_e32 v67, v13, v13
	v_max_f32_e32 v68, v12, v12
	v_max_f32_e32 v67, v68, v67
	v_max3_f32 v33, v33, v66, v67
	v_max_f32_e32 v66, v15, v15
	v_max_f32_e32 v67, v14, v14
	v_max_f32_e32 v66, v67, v66
	v_max_f32_e32 v67, v17, v17
	v_max_f32_e32 v68, v16, v16
	v_max_f32_e32 v67, v68, v67
	v_max3_f32 v33, v33, v66, v67
	v_max_f32_e32 v66, v35, v35
	v_max_f32_e32 v67, v34, v34
	v_max_f32_e32 v66, v67, v66
	v_max_f32_e32 v67, v37, v37
	v_max_f32_e32 v68, v36, v36
	v_max_f32_e32 v67, v68, v67
	v_max3_f32 v33, v33, v66, v67
	v_max_f32_e32 v66, v39, v39
	v_max_f32_e32 v67, v38, v38
	v_max_f32_e32 v66, v67, v66
	v_max_f32_e32 v67, v41, v41
	v_max_f32_e32 v68, v40, v40
	v_max_f32_e32 v67, v68, v67
	v_max3_f32 v33, v33, v66, v67
	v_max_f32_e32 v66, v43, v43
	v_max_f32_e32 v67, v42, v42
	v_max_f32_e32 v66, v67, v66
	v_max_f32_e32 v67, v45, v45
	v_max_f32_e32 v68, v44, v44
	v_max_f32_e32 v67, v68, v67
	v_max3_f32 v33, v33, v66, v67
	v_max_f32_e32 v66, v47, v47
	v_max_f32_e32 v67, v46, v46
	v_max_f32_e32 v66, v67, v66
	v_max_f32_e32 v67, v49, v49
	v_max_f32_e32 v68, v48, v48
	v_max_f32_e32 v67, v68, v67
	v_max3_f32 v33, v33, v66, v67
	v_max_f32_e32 v66, v51, v51
	v_max_f32_e32 v67, v50, v50
	v_max_f32_e32 v66, v67, v66
	v_max_f32_e32 v67, v53, v53
	v_max_f32_e32 v68, v52, v52
	v_max_f32_e32 v67, v68, v67
	v_max3_f32 v33, v33, v66, v67
	v_max_f32_e32 v66, v55, v55
	v_max_f32_e32 v67, v54, v54
	v_max_f32_e32 v66, v67, v66
	v_max_f32_e32 v67, v57, v57
	v_max_f32_e32 v68, v56, v56
	v_max_f32_e32 v67, v68, v67
	v_max3_f32 v33, v33, v66, v67
	v_max_f32_e32 v66, v59, v59
	v_max_f32_e32 v67, v58, v58
	v_max_f32_e32 v66, v67, v66
	v_max_f32_e32 v67, v61, v61
	v_max_f32_e32 v68, v60, v60
	v_max_f32_e32 v67, v68, v67
	v_max3_f32 v33, v33, v66, v67
	v_max_f32_e32 v66, v63, v63
	v_max_f32_e32 v67, v62, v62
	v_max_f32_e32 v66, v67, v66
	v_max_f32_e32 v67, v65, v65
	v_max_f32_e32 v68, v64, v64
	v_max_f32_e32 v67, v68, v67
	v_max3_f32 v33, v33, v66, v67
	v_max_f32_e32 v66, v83, v83
	v_max_f32_e32 v67, v82, v82
	v_max_f32_e32 v66, v67, v66
	v_max_f32_e32 v67, v85, v85
	v_max_f32_e32 v68, v84, v84
	v_max_f32_e32 v67, v68, v67
	v_max3_f32 v33, v33, v66, v67
	v_max_f32_e32 v66, v87, v87
	v_max_f32_e32 v67, v86, v86
	v_max_f32_e32 v66, v67, v66
	v_max_f32_e32 v67, v89, v89
	v_max_f32_e32 v68, v88, v88
	v_max_f32_e32 v67, v68, v67
	v_max3_f32 v33, v33, v66, v67
	v_max_f32_e32 v66, v91, v91
	v_max_f32_e32 v67, v90, v90
	v_max_f32_e32 v66, v67, v66
	v_max_f32_e32 v67, v93, v93
	v_max_f32_e32 v68, v92, v92
	v_max_f32_e32 v67, v68, v67
	v_cndmask_b32_e64 v70, v81, v226, s[78:79]
	v_max3_f32 v33, v33, v66, v67
	v_max_f32_e32 v66, v95, v95
	v_max_f32_e32 v67, v94, v94
	v_max_f32_e32 v66, v67, v66
	v_max_f32_e32 v67, v70, v70
	v_max_f32_e32 v68, v96, v96
	v_max_f32_e32 v67, v68, v67
	v_max3_f32 v33, v33, v66, v67
	v_and_b32_e32 v67, 64, v209
	v_xor_b32_e32 v66, 32, v209
	v_add_u32_e32 v67, 64, v67
	v_cmp_lt_i32_e32 vcc, v66, v67
	s_nop 1
	v_cndmask_b32_e32 v66, v209, v66, vcc
	v_lshlrev_b32_e32 v118, 2, v66
	ds_bpermute_b32 v66, v118, v33
	s_waitcnt lgkmcnt(0)
	v_max_f32_e32 v66, v66, v66
	v_max_f32_e32 v66, v33, v66
	v_sub_f32_e32 v33, v97, v66
	v_exp_f32_e32 v33, v33
	v_sub_f32_e32 v18, v18, v66
	v_exp_f32_e32 v18, v18
	v_sub_f32_e32 v19, v19, v66
	v_exp_f32_e32 v19, v19
	v_sub_f32_e32 v20, v20, v66
	v_exp_f32_e32 v20, v20
	v_sub_f32_e32 v21, v21, v66
	v_add_f32_e32 v67, 0, v33
	v_exp_f32_e32 v21, v21
	v_sub_f32_e32 v22, v22, v66
	v_add_f32_e32 v67, v18, v67
	v_exp_f32_e32 v22, v22
	v_sub_f32_e32 v23, v23, v66
	v_add_f32_e32 v67, v19, v67
	v_exp_f32_e32 v23, v23
	v_sub_f32_e32 v24, v24, v66
	v_add_f32_e32 v67, v20, v67
	v_exp_f32_e32 v24, v24
	v_sub_f32_e32 v25, v25, v66
	v_add_f32_e32 v67, v21, v67
	v_exp_f32_e32 v119, v25
	v_sub_f32_e32 v25, v26, v66
	v_add_f32_e32 v67, v22, v67
	v_exp_f32_e32 v120, v25
	v_sub_f32_e32 v25, v27, v66
	v_add_f32_e32 v67, v23, v67
	v_exp_f32_e32 v121, v25
	v_sub_f32_e32 v26, v28, v66
	v_add_f32_e32 v25, v24, v67
	v_exp_f32_e32 v122, v26
	v_sub_f32_e32 v26, v29, v66
	v_add_f32_e32 v25, v119, v25
	v_exp_f32_e32 v123, v26
	v_sub_f32_e32 v26, v31, v66
	v_add_f32_e32 v25, v120, v25
	v_exp_f32_e32 v124, v26
	v_sub_f32_e32 v26, v32, v66
	v_add_f32_e32 v25, v121, v25
	v_exp_f32_e32 v125, v26
	v_sub_f32_e32 v26, v30, v66
	v_add_f32_e32 v25, v122, v25
	v_exp_f32_e32 v126, v26
	v_sub_f32_e32 v2, v2, v66
	v_add_f32_e32 v25, v123, v25
	v_exp_f32_e32 v103, v2
	v_sub_f32_e32 v2, v3, v66
	v_add_f32_e32 v25, v124, v25
	v_exp_f32_e32 v106, v2
	v_sub_f32_e32 v2, v4, v66
	v_add_f32_e32 v25, v125, v25
	v_exp_f32_e32 v107, v2
	v_sub_f32_e32 v3, v5, v66
	v_add_f32_e32 v2, v126, v25
	v_exp_f32_e32 v110, v3
	v_sub_f32_e32 v3, v6, v66
	v_add_f32_e32 v2, v103, v2
	v_exp_f32_e32 v111, v3
	v_sub_f32_e32 v3, v7, v66
	v_add_f32_e32 v2, v106, v2
	v_exp_f32_e32 v114, v3
	v_sub_f32_e32 v3, v8, v66
	v_add_f32_e32 v2, v107, v2
	v_exp_f32_e32 v115, v3
	v_sub_f32_e32 v3, v9, v66
	v_add_f32_e32 v2, v110, v2
	v_exp_f32_e32 v117, v3
	v_sub_f32_e32 v3, v10, v66
	v_add_f32_e32 v2, v111, v2
	v_exp_f32_e32 v102, v3
	v_sub_f32_e32 v3, v11, v66
	v_add_f32_e32 v2, v114, v2
	v_exp_f32_e32 v104, v3
	v_sub_f32_e32 v3, v12, v66
	v_add_f32_e32 v2, v115, v2
	v_exp_f32_e32 v105, v3
	v_sub_f32_e32 v3, v13, v66
	v_add_f32_e32 v2, v117, v2
	v_exp_f32_e32 v108, v3
	v_sub_f32_e32 v3, v14, v66
	v_add_f32_e32 v2, v102, v2
	v_exp_f32_e32 v109, v3
	v_sub_f32_e32 v3, v15, v66
	v_add_f32_e32 v2, v104, v2
	v_exp_f32_e32 v112, v3
	v_sub_f32_e32 v3, v16, v66
	v_add_f32_e32 v2, v105, v2
	v_exp_f32_e32 v113, v3
	v_sub_f32_e32 v3, v17, v66
	v_add_f32_e32 v2, v108, v2
	v_exp_f32_e32 v116, v3
	v_sub_f32_e32 v3, v34, v66
	v_add_f32_e32 v2, v109, v2
	v_exp_f32_e32 v72, v3
	v_sub_f32_e32 v3, v35, v66
	v_add_f32_e32 v2, v112, v2
	v_exp_f32_e32 v75, v3
	v_sub_f32_e32 v3, v36, v66
	v_add_f32_e32 v2, v113, v2
	v_exp_f32_e32 v76, v3
	v_sub_f32_e32 v3, v37, v66
	v_add_f32_e32 v2, v116, v2
	v_exp_f32_e32 v79, v3
	v_sub_f32_e32 v3, v38, v66
	v_add_f32_e32 v2, v72, v2
	v_exp_f32_e32 v80, v3
	v_sub_f32_e32 v3, v39, v66
	v_add_f32_e32 v2, v75, v2
	v_exp_f32_e32 v98, v3
	v_sub_f32_e32 v3, v40, v66
	v_add_f32_e32 v2, v76, v2
	v_exp_f32_e32 v99, v3
	v_sub_f32_e32 v3, v41, v66
	v_add_f32_e32 v2, v79, v2
	v_exp_f32_e32 v101, v3
	v_sub_f32_e32 v3, v42, v66
	v_add_f32_e32 v2, v80, v2
	v_exp_f32_e32 v71, v3
	v_sub_f32_e32 v3, v43, v66
	v_add_f32_e32 v2, v98, v2
	v_exp_f32_e32 v73, v3
	v_sub_f32_e32 v3, v44, v66
	v_add_f32_e32 v2, v99, v2
	v_exp_f32_e32 v74, v3
	v_sub_f32_e32 v3, v45, v66
	v_add_f32_e32 v2, v101, v2
	v_exp_f32_e32 v77, v3
	v_sub_f32_e32 v3, v46, v66
	v_add_f32_e32 v2, v71, v2
	v_exp_f32_e32 v78, v3
	v_sub_f32_e32 v3, v47, v66
	v_add_f32_e32 v2, v73, v2
	v_exp_f32_e32 v81, v3
	v_sub_f32_e32 v3, v48, v66
	v_add_f32_e32 v2, v74, v2
	v_exp_f32_e32 v97, v3
	v_sub_f32_e32 v3, v49, v66
	v_add_f32_e32 v2, v77, v2
	v_exp_f32_e32 v100, v3
	v_sub_f32_e32 v3, v50, v66
	v_add_f32_e32 v2, v78, v2
	v_exp_f32_e32 v41, v3
	v_sub_f32_e32 v3, v51, v66
	v_add_f32_e32 v2, v81, v2
	v_exp_f32_e32 v46, v3
	v_sub_f32_e32 v3, v52, v66
	v_add_f32_e32 v2, v97, v2
	v_exp_f32_e32 v47, v3
	v_sub_f32_e32 v3, v53, v66
	v_add_f32_e32 v2, v100, v2
	v_exp_f32_e32 v53, v3
	v_sub_f32_e32 v3, v54, v66
	v_add_f32_e32 v2, v41, v2
	v_exp_f32_e32 v54, v3
	v_sub_f32_e32 v3, v55, v66
	v_add_f32_e32 v2, v46, v2
	v_exp_f32_e32 v67, v3
	v_sub_f32_e32 v3, v56, v66
	v_add_f32_e32 v2, v47, v2
	v_exp_f32_e32 v68, v3
	v_sub_f32_e32 v3, v57, v66
	v_add_f32_e32 v2, v53, v2
	v_exp_f32_e32 v69, v3
	v_sub_f32_e32 v3, v58, v66
	v_add_f32_e32 v2, v54, v2
	v_exp_f32_e32 v38, v3
	v_sub_f32_e32 v3, v59, v66
	v_add_f32_e32 v2, v67, v2
	v_exp_f32_e32 v44, v3
	v_sub_f32_e32 v3, v60, v66
	v_add_f32_e32 v2, v68, v2
	v_exp_f32_e32 v45, v3
	v_sub_f32_e32 v3, v61, v66
	v_add_f32_e32 v2, v69, v2
	v_exp_f32_e32 v51, v3
	v_sub_f32_e32 v3, v62, v66
	v_add_f32_e32 v2, v38, v2
	v_exp_f32_e32 v52, v3
	v_sub_f32_e32 v3, v63, v66
	v_add_f32_e32 v2, v44, v2
	v_exp_f32_e32 v57, v3
	v_sub_f32_e32 v3, v64, v66
	v_add_f32_e32 v2, v45, v2
	v_exp_f32_e32 v58, v3
	v_sub_f32_e32 v3, v65, v66
	v_add_f32_e32 v2, v51, v2
	v_exp_f32_e32 v62, v3
	v_sub_f32_e32 v3, v82, v66
	v_add_f32_e32 v2, v52, v2
	v_exp_f32_e32 v37, v3
	v_sub_f32_e32 v3, v83, v66
	v_add_f32_e32 v2, v57, v2
	v_exp_f32_e32 v42, v3
	v_sub_f32_e32 v3, v84, v66
	v_add_f32_e32 v2, v58, v2
	v_exp_f32_e32 v43, v3
	v_sub_f32_e32 v3, v85, v66
	v_add_f32_e32 v2, v62, v2
	v_exp_f32_e32 v49, v3
	v_sub_f32_e32 v3, v86, v66
	v_add_f32_e32 v2, v37, v2
	v_exp_f32_e32 v50, v3
	v_sub_f32_e32 v3, v87, v66
	v_add_f32_e32 v2, v42, v2
	v_exp_f32_e32 v55, v3
	v_sub_f32_e32 v3, v88, v66
	v_add_f32_e32 v2, v43, v2
	v_exp_f32_e32 v56, v3
	v_sub_f32_e32 v3, v89, v66
	v_add_f32_e32 v2, v49, v2
	v_exp_f32_e32 v61, v3
	v_sub_f32_e32 v3, v90, v66
	v_add_f32_e32 v2, v50, v2
	v_exp_f32_e32 v36, v3
	v_sub_f32_e32 v3, v91, v66
	v_add_f32_e32 v2, v55, v2
	v_exp_f32_e32 v39, v3
	v_sub_f32_e32 v3, v92, v66
	v_add_f32_e32 v2, v56, v2
	v_exp_f32_e32 v40, v3
	v_add_f32_e32 v2, v61, v2
	v_add_f32_e32 v2, v36, v2
	v_add_f32_e32 v2, v39, v2
	v_add_f32_e32 v14, v40, v2
	v_sub_f32_e32 v2, v93, v66
	v_exp_f32_e32 v48, v2
	v_cvt_pk_bf16_f32 v2, v33, v18
	v_cvt_pk_bf16_f32 v3, v19, v20
	v_cvt_pk_bf16_f32 v4, v21, v22
	v_cvt_pk_bf16_f32 v5, v23, v24
	ds_read_b64_tr_b16 v[10:11], v195
	ds_read_b64_tr_b16 v[12:13], v195 offset:1024
	ds_read_b64_tr_b16 v[6:7], v196
	ds_read_b64_tr_b16 v[8:9], v196 offset:1024
	s_waitcnt lgkmcnt(0)
	s_nop 0
	v_add_f32_e32 v34, v48, v14
	v_mfma_f32_32x32x16_bf16 v[18:33], v[10:13], v[2:5], 0
	v_sub_f32_e32 v10, v94, v66
	v_exp_f32_e32 v63, v10
	v_sub_f32_e32 v10, v95, v66
	v_exp_f32_e32 v65, v10
	v_sub_f32_e32 v10, v96, v66
	v_exp_f32_e32 v64, v10
	v_sub_f32_e32 v35, v70, v66
	v_mfma_f32_32x32x16_bf16 v[2:17], v[6:9], v[2:5], 0
	v_exp_f32_e32 v70, v35
	v_add_f32_e32 v34, v63, v34
	v_cvt_pk_bf16_f32 v82, v119, v120
	v_cvt_pk_bf16_f32 v83, v121, v122
	v_cvt_pk_bf16_f32 v84, v123, v124
	v_cvt_pk_bf16_f32 v85, v125, v126
	ds_read_b64_tr_b16 v[90:91], v197
	ds_read_b64_tr_b16 v[92:93], v197 offset:1024
	ds_read_b64_tr_b16 v[86:87], v198
	ds_read_b64_tr_b16 v[88:89], v198 offset:1024
	s_waitcnt lgkmcnt(0)
	v_add_f32_e32 v34, v65, v34
	v_mfma_f32_32x32x16_bf16 v[18:33], v[90:93], v[82:85], v[18:33]
	v_add_f32_e32 v34, v64, v34
	v_add_f32_e32 v59, v70, v34
	ds_bpermute_b32 v60, v118, v59
	v_mfma_f32_32x32x16_bf16 v[2:17], v[86:89], v[82:85], v[2:17]
	s_and_b64 vcc, exec, s[72:73]
	s_mov_b64 s[4:5], -1
	s_cbranch_vccnz .LBB0_473
	v_mov_b32_e32 v84, v0
	s_lshl_b32 s90, s37, 1
	v_bfe_u32 v86, v84, 3, 3
	v_or_b32_e32 v34, s2, v86
	v_mul_lo_u32 v34, v34, s81
	v_add_u32_e32 v34, s82, v34
	v_max_i32_e32 v82, 0, v34
	v_mov_b64_e32 v[34:35], s[84:85]
	v_mad_u64_u32 v[82:83], s[4:5], v82, s21, v[34:35]
	v_lshlrev_b32_e32 v84, 4, v84
	v_lshl_add_u64 v[82:83], v[82:83], 0, s[90:91]
	v_and_b32_e32 v84, 0x70, v84
	v_mov_b32_e32 v85, v179
	v_lshl_add_u64 v[82:83], v[82:83], 0, v[84:85]
	s_mov_b32 m0, s75
	v_lshl_add_u64 v[82:83], v[82:83], 0, s[94:95]
	v_or_b32_e32 v82, s10, v86
	v_mul_lo_u32 v82, v82, s81
	v_add_u32_e32 v82, s82, v82
	v_max_i32_e32 v82, 0, v82
	v_mad_u64_u32 v[82:83], s[4:5], v82, s21, v[34:35]
	v_lshl_add_u64 v[82:83], v[82:83], 0, s[90:91]
	v_lshl_add_u64 v[82:83], v[82:83], 0, v[84:85]
	v_lshl_add_u64 v[82:83], v[82:83], 0, s[94:95]
	s_mov_b32 m0, s26
	s_nop 0
	v_or_b32_e32 v82, s11, v86
	v_mul_lo_u32 v82, v82, s81
	v_add_u32_e32 v82, s82, v82
	v_max_i32_e32 v82, 0, v82
	v_mad_u64_u32 v[82:83], s[4:5], v82, s21, v[34:35]
	v_lshl_add_u64 v[82:83], v[82:83], 0, s[90:91]
	v_lshl_add_u64 v[82:83], v[82:83], 0, v[84:85]
	v_lshl_add_u64 v[82:83], v[82:83], 0, s[94:95]
	s_add_i32 m0, s75, 0x800
	s_nop 0
	v_or_b32_e32 v82, s12, v86
	v_mul_lo_u32 v82, v82, s81
	v_add_u32_e32 v82, s82, v82
	v_max_i32_e32 v82, 0, v82
	v_mad_u64_u32 v[34:35], s[4:5], v82, s21, v[34:35]
	v_lshl_add_u64 v[34:35], v[34:35], 0, s[90:91]
	v_lshl_add_u64 v[34:35], v[34:35], 0, v[84:85]
	v_lshl_add_u64 v[34:35], v[34:35], 0, s[94:95]
	s_mov_b64 s[4:5], 0
.LBB0_473:
	s_andn2_b64 vcc, exec, s[4:5]
	s_cbranch_vccnz .LBB0_475
	s_lshl_b32 s4, s81, 6
	s_mov_b32 m0, s75
	v_mad_i64_i32 v[34:35], s[4:5], s4, v225, v[188:189]
	v_mad_i64_i32 v[34:35], s[4:5], s89, v225, v[188:189]
	s_mov_b32 m0, s26
	s_nop 0
	v_mad_i64_i32 v[34:35], s[4:5], s87, v225, v[188:189]
	s_add_i32 m0, s75, 0x800
	s_nop 0
	v_mad_i64_i32 v[34:35], s[4:5], s43, v225, v[188:189]
.LBB0_475:
	s_mov_b32 m0, s27
	s_nop 0
	v_cvt_pk_bf16_f32 v82, v103, v106
	v_cvt_pk_bf16_f32 v83, v107, v110
	v_cvt_pk_bf16_f32 v84, v111, v114
	v_cvt_pk_bf16_f32 v85, v115, v117
	ds_read_b64_tr_b16 v[90:91], v199
	ds_read_b64_tr_b16 v[92:93], v199 offset:1024
	ds_read_b64_tr_b16 v[86:87], v200
	ds_read_b64_tr_b16 v[88:89], v200 offset:1024
	s_waitcnt lgkmcnt(0)
	s_nop 0
	v_mfma_f32_32x32x16_bf16 v[18:33], v[90:93], v[82:85], v[18:33]
	v_mfma_f32_32x32x16_bf16 v[2:17], v[86:89], v[82:85], v[2:17]
	v_cvt_pk_bf16_f32 v82, v102, v104
	v_cvt_pk_bf16_f32 v83, v105, v108
	v_cvt_pk_bf16_f32 v84, v109, v112
	v_cvt_pk_bf16_f32 v85, v113, v116
	ds_read_b64_tr_b16 v[90:91], v201
	ds_read_b64_tr_b16 v[92:93], v201 offset:1024
	ds_read_b64_tr_b16 v[86:87], v202
	ds_read_b64_tr_b16 v[88:89], v202 offset:1024
	s_waitcnt lgkmcnt(0)
	s_nop 0
	v_mfma_f32_32x32x16_bf16 v[18:33], v[90:93], v[82:85], v[18:33]
	v_mfma_f32_32x32x16_bf16 v[2:17], v[86:89], v[82:85], v[2:17]
	s_and_b64 vcc, exec, s[72:73]
	s_mov_b64 s[4:5], -1
	s_cbranch_vccnz .LBB0_477
	v_mov_b32_e32 v84, v0
	s_lshl_b32 s90, s37, 1
	v_bfe_u32 v86, v84, 3, 3
	v_or_b32_e32 v34, s13, v86
	v_mul_lo_u32 v34, v34, s81
	v_add_u32_e32 v34, s82, v34
	v_max_i32_e32 v82, 0, v34
	v_mov_b64_e32 v[34:35], s[84:85]
	v_mad_u64_u32 v[82:83], s[4:5], v82, s21, v[34:35]
	v_lshlrev_b32_e32 v84, 4, v84
	v_lshl_add_u64 v[82:83], v[82:83], 0, s[90:91]
	v_and_b32_e32 v84, 0x70, v84
	v_mov_b32_e32 v85, v179
	v_lshl_add_u64 v[82:83], v[82:83], 0, v[84:85]
	s_mov_b32 m0, s83
	v_lshl_add_u64 v[82:83], v[82:83], 0, s[94:95]
	v_or_b32_e32 v82, s14, v86
	v_mul_lo_u32 v82, v82, s81
	v_add_u32_e32 v82, s82, v82
	v_max_i32_e32 v82, 0, v82
	v_mad_u64_u32 v[82:83], s[4:5], v82, s21, v[34:35]
	v_lshl_add_u64 v[82:83], v[82:83], 0, s[90:91]
	v_lshl_add_u64 v[82:83], v[82:83], 0, v[84:85]
	v_lshl_add_u64 v[82:83], v[82:83], 0, s[94:95]
	s_mov_b32 m0, s28
	s_nop 0
	v_or_b32_e32 v82, s15, v86
	v_mul_lo_u32 v82, v82, s81
	v_add_u32_e32 v82, s82, v82
	v_max_i32_e32 v82, 0, v82
	v_mad_u64_u32 v[82:83], s[4:5], v82, s21, v[34:35]
	v_lshl_add_u64 v[82:83], v[82:83], 0, s[90:91]
	v_lshl_add_u64 v[82:83], v[82:83], 0, v[84:85]
	v_lshl_add_u64 v[82:83], v[82:83], 0, s[94:95]
	s_mov_b32 m0, s29
	s_nop 0
	v_or_b32_e32 v82, s16, v86
	v_mul_lo_u32 v82, v82, s81
	v_add_u32_e32 v82, s82, v82
	v_max_i32_e32 v82, 0, v82
	v_mad_u64_u32 v[34:35], s[4:5], v82, s21, v[34:35]
	v_lshl_add_u64 v[34:35], v[34:35], 0, s[90:91]
	v_lshl_add_u64 v[34:35], v[34:35], 0, v[84:85]
	v_lshl_add_u64 v[34:35], v[34:35], 0, s[94:95]
	s_mov_b64 s[4:5], 0
.LBB0_477:
	s_andn2_b64 vcc, exec, s[4:5]
	s_cbranch_vccnz .LBB0_479
	s_mov_b32 m0, s83
	v_mad_i64_i32 v[34:35], s[4:5], s52, v225, v[188:189]
	v_mad_i64_i32 v[34:35], s[4:5], s51, v225, v[188:189]
	s_mov_b32 m0, s28
	s_nop 0
	v_mad_i64_i32 v[34:35], s[4:5], s50, v225, v[188:189]
	s_mov_b32 m0, s29
	s_nop 0
	v_mad_i64_i32 v[34:35], s[4:5], s49, v225, v[188:189]
.LBB0_479:
	s_mov_b32 m0, s30
	s_nop 0
	v_cvt_pk_bf16_f32 v82, v72, v75
	v_cvt_pk_bf16_f32 v83, v76, v79
	v_cvt_pk_bf16_f32 v84, v80, v98
	v_cvt_pk_bf16_f32 v85, v99, v101
	ds_read_b64_tr_b16 v[90:91], v195 offset:8192
	ds_read_b64_tr_b16 v[92:93], v195 offset:9216
	ds_read_b64_tr_b16 v[86:87], v196 offset:8192
	ds_read_b64_tr_b16 v[88:89], v196 offset:9216
	s_waitcnt lgkmcnt(0)
	v_cvt_pk_bf16_f32 v72, v71, v73
	v_cvt_pk_bf16_f32 v73, v74, v77
	v_cvt_pk_bf16_f32 v74, v78, v81
	v_cvt_pk_bf16_f32 v75, v97, v100
	s_nop 0
	v_mfma_f32_32x32x16_bf16 v[18:33], v[90:93], v[82:85], v[18:33]
	v_mfma_f32_32x32x16_bf16 v[2:17], v[86:89], v[82:85], v[2:17]
	ds_read_b64_tr_b16 v[80:81], v197 offset:8192
	ds_read_b64_tr_b16 v[82:83], v197 offset:9216
	ds_read_b64_tr_b16 v[76:77], v198 offset:8192
	ds_read_b64_tr_b16 v[78:79], v198 offset:9216
	s_waitcnt lgkmcnt(0)
	s_nop 0
	v_mfma_f32_32x32x16_bf16 v[18:33], v[80:83], v[72:75], v[18:33]
	v_mfma_f32_32x32x16_bf16 v[2:17], v[76:79], v[72:75], v[2:17]
	s_and_b64 vcc, exec, s[72:73]
	s_mov_b64 s[4:5], -1
	s_cbranch_vccnz .LBB0_481
	v_mov_b32_e32 v71, v0
	s_lshl_b32 s90, s37, 1
	v_bfe_u32 v76, v71, 3, 3
	v_or_b32_e32 v34, s17, v76
	v_mul_lo_u32 v34, v34, s81
	v_add_u32_e32 v34, s82, v34
	v_max_i32_e32 v72, 0, v34
	v_mov_b64_e32 v[34:35], s[84:85]
	v_lshlrev_b32_e32 v71, 4, v71
	v_mad_u64_u32 v[72:73], s[4:5], v72, s21, v[34:35]
	v_and_b32_e32 v74, 0x70, v71
	v_or_b32_e32 v71, s18, v76
	v_lshl_add_u64 v[72:73], v[72:73], 0, s[90:91]
	v_mov_b32_e32 v75, v179
	v_mul_lo_u32 v71, v71, s81
	v_lshl_add_u64 v[72:73], v[72:73], 0, v[74:75]
	v_add_u32_e32 v71, s82, v71
	s_mov_b32 m0, s75
	v_lshl_add_u64 v[72:73], v[72:73], 0, s[94:95]
	v_max_i32_e32 v71, 0, v71
	v_mad_u64_u32 v[72:73], s[4:5], v71, s21, v[34:35]
	v_or_b32_e32 v71, s19, v76
	v_lshl_add_u64 v[72:73], v[72:73], 0, s[90:91]
	v_mul_lo_u32 v71, v71, s81
	v_lshl_add_u64 v[72:73], v[72:73], 0, v[74:75]
	v_add_u32_e32 v71, s82, v71
	v_lshl_add_u64 v[72:73], v[72:73], 0, s[94:95]
	s_mov_b32 m0, s26
	v_max_i32_e32 v71, 0, v71
	v_mad_u64_u32 v[72:73], s[4:5], v71, s21, v[34:35]
	v_lshl_add_u64 v[72:73], v[72:73], 0, s[90:91]
	v_lshl_add_u64 v[72:73], v[72:73], 0, v[74:75]
	v_lshl_add_u64 v[72:73], v[72:73], 0, s[94:95]
	s_add_i32 m0, s75, 0x800
	v_or_b32_e32 v71, s20, v76
	v_mul_lo_u32 v71, v71, s81
	v_add_u32_e32 v71, s82, v71
	v_max_i32_e32 v71, 0, v71
	v_mad_u64_u32 v[34:35], s[4:5], v71, s21, v[34:35]
	v_lshl_add_u64 v[34:35], v[34:35], 0, s[90:91]
	v_lshl_add_u64 v[34:35], v[34:35], 0, v[74:75]
	v_lshl_add_u64 v[34:35], v[34:35], 0, s[94:95]
	s_mov_b64 s[4:5], 0
.LBB0_481:
	s_andn2_b64 vcc, exec, s[4:5]
	s_cbranch_vccnz .LBB0_483
	s_lshl_b32 s4, s81, 7
	s_mov_b32 m0, s75
	v_mad_i64_i32 v[34:35], s[4:5], s4, v225, v[188:189]
	v_mad_i64_i32 v[34:35], s[4:5], s46, v225, v[188:189]
	s_mov_b32 m0, s26
	s_nop 0
	v_mad_i64_i32 v[34:35], s[4:5], s45, v225, v[188:189]
	s_add_i32 m0, s75, 0x800
	s_nop 0
	v_mad_i64_i32 v[34:35], s[4:5], s44, v225, v[188:189]
.LBB0_483:
	s_mov_b32 m0, s27
	s_andn2_b64 vcc, exec, s[96:97]
	v_cvt_pk_bf16_f32 v72, v41, v46
	v_cvt_pk_bf16_f32 v73, v47, v53
	v_cvt_pk_bf16_f32 v74, v54, v67
	v_cvt_pk_bf16_f32 v75, v68, v69
	ds_read_b64_tr_b16 v[80:81], v199 offset:8192
	ds_read_b64_tr_b16 v[82:83], v199 offset:9216
	ds_read_b64_tr_b16 v[76:77], v200 offset:8192
	ds_read_b64_tr_b16 v[78:79], v200 offset:9216
	s_waitcnt lgkmcnt(0)
	v_cvt_pk_bf16_f32 v44, v38, v44
	v_cvt_pk_bf16_f32 v45, v45, v51
	v_cvt_pk_bf16_f32 v46, v52, v57
	v_cvt_pk_bf16_f32 v47, v58, v62
	s_nop 0
	v_mfma_f32_32x32x16_bf16 v[18:33], v[80:83], v[72:75], v[18:33]
	v_mfma_f32_32x32x16_bf16 v[2:17], v[76:79], v[72:75], v[2:17]
	ds_read_b64_tr_b16 v[76:77], v201 offset:8192
	ds_read_b64_tr_b16 v[78:79], v201 offset:9216
	ds_read_b64_tr_b16 v[72:73], v202 offset:8192
	ds_read_b64_tr_b16 v[74:75], v202 offset:9216
	s_waitcnt lgkmcnt(0)
	v_cvt_pk_bf16_f32 v42, v37, v42
	v_cvt_pk_bf16_f32 v43, v43, v49
	s_nop 0
	v_mfma_f32_32x32x16_bf16 v[18:33], v[76:79], v[44:47], v[18:33]
	v_mfma_f32_32x32x16_bf16 v[2:17], v[72:75], v[44:47], v[2:17]
	v_cvt_pk_bf16_f32 v44, v50, v55
	v_cvt_pk_bf16_f32 v45, v56, v61
	ds_read_b64_tr_b16 v[54:55], v195 offset:16384
	ds_read_b64_tr_b16 v[56:57], v195 offset:17408
	ds_read_b64_tr_b16 v[50:51], v196 offset:16384
	ds_read_b64_tr_b16 v[52:53], v196 offset:17408
	s_waitcnt lgkmcnt(0)
	v_cvt_pk_bf16_f32 v34, v36, v39
	v_cvt_pk_bf16_f32 v35, v40, v48
	v_cvt_pk_bf16_f32 v36, v63, v65
	v_cvt_pk_bf16_f32 v37, v64, v70
	s_nop 0
	v_mfma_f32_32x32x16_bf16 v[18:33], v[54:57], v[42:45], v[18:33]
	v_mfma_f32_32x32x16_bf16 v[2:17], v[50:53], v[42:45], v[2:17]
	ds_read_b64_tr_b16 v[42:43], v197 offset:16384
	ds_read_b64_tr_b16 v[44:45], v197 offset:17408
	ds_read_b64_tr_b16 v[38:39], v198 offset:16384
	ds_read_b64_tr_b16 v[40:41], v198 offset:17408
	s_waitcnt lgkmcnt(0)
	s_nop 0
	v_mfma_f32_32x32x16_bf16 v[18:33], v[42:45], v[34:37], v[18:33]
	v_cndmask_b32_e64 v42, 0, 1, s[96:97]
	v_cmp_ne_u32_e64 s[72:73], 1, v42
	v_mfma_f32_32x32x16_bf16 v[2:17], v[38:41], v[34:37], v[2:17]
	s_cbranch_vccnz .LBB0_485
	s_waitcnt vmcnt(0)
.LBB0_485:
	s_waitcnt vmcnt(0)
	s_barrier
	s_waitcnt lgkmcnt(0)
	v_add_f32_e32 v34, v59, v60
	v_div_scale_f32 v35, s[4:5], v34, v34, 1.0
	v_rcp_f32_e32 v36, v35
	v_div_scale_f32 v37, vcc, 1.0, v34, 1.0
	s_ashr_i32 s87, s86, 31
	v_fma_f32 v38, -v35, v36, 1.0
	v_fmac_f32_e32 v36, v38, v36
	v_mul_f32_e32 v38, v37, v36
	v_fma_f32 v39, -v35, v38, v37
	v_fmac_f32_e32 v38, v39, v36
	v_fma_f32 v35, -v35, v38, v37
	v_div_fmas_f32 v35, v35, v36, v38
	v_div_fixup_f32 v35, v35, v34, 1.0
	v_mul_f32_e32 v18, v35, v18
	v_mul_f32_e32 v19, v35, v19
	v_cvt_pk_bf16_f32 v18, v18, v19
	v_mul_f32_e32 v19, v35, v20
	v_mul_f32_e32 v20, v35, v21
	v_cvt_pk_bf16_f32 v19, v19, v20
	v_add_u32_e32 v20, v194, v193
	ds_write_b64 v20, v[18:19] offset:4096
	v_mul_f32_e32 v18, v35, v22
	v_mul_f32_e32 v19, v35, v23
	v_cvt_pk_bf16_f32 v18, v18, v19
	v_mul_f32_e32 v19, v35, v24
	v_mul_f32_e32 v20, v35, v25
	v_cvt_pk_bf16_f32 v19, v19, v20
	ds_write_b64 v210, v[18:19] offset:4096
	v_mul_f32_e32 v18, v35, v26
	v_mul_f32_e32 v19, v35, v27
	v_cvt_pk_bf16_f32 v18, v18, v19
	v_mul_f32_e32 v19, v35, v28
	v_mul_f32_e32 v20, v35, v29
	v_cvt_pk_bf16_f32 v19, v19, v20
	ds_write_b64 v211, v[18:19] offset:4096
	v_mul_f32_e32 v18, v35, v30
	v_mul_f32_e32 v19, v35, v31
	v_cvt_pk_bf16_f32 v18, v18, v19
	v_mul_f32_e32 v19, v35, v32
	v_mul_f32_e32 v2, v35, v2
	v_mul_f32_e32 v3, v35, v3
	v_mul_f32_e32 v20, v35, v33
	v_cvt_pk_bf16_f32 v19, v19, v20
	ds_write_b64 v212, v[18:19] offset:4096
	v_cvt_pk_bf16_f32 v2, v2, v3
	v_mul_f32_e32 v3, v35, v4
	v_mul_f32_e32 v4, v35, v5
	v_cvt_pk_bf16_f32 v3, v3, v4
	ds_write_b64 v213, v[2:3] offset:4096
	v_mul_f32_e32 v2, v35, v6
	v_mul_f32_e32 v3, v35, v7
	v_cvt_pk_bf16_f32 v2, v2, v3
	v_mul_f32_e32 v3, v35, v8
	v_mul_f32_e32 v4, v35, v9
	v_cvt_pk_bf16_f32 v3, v3, v4
	ds_write_b64 v214, v[2:3] offset:4096
	v_mul_f32_e32 v2, v35, v10
	v_mul_f32_e32 v3, v35, v11
	v_cvt_pk_bf16_f32 v2, v2, v3
	v_mul_f32_e32 v3, v35, v12
	v_mul_f32_e32 v4, v35, v13
	v_cvt_pk_bf16_f32 v3, v3, v4
	ds_write_b64 v215, v[2:3] offset:4096
	v_mul_f32_e32 v2, v35, v14
	v_mul_f32_e32 v3, v35, v15
	v_cvt_pk_bf16_f32 v2, v2, v3
	v_mul_f32_e32 v3, v35, v16
	v_mul_f32_e32 v4, v35, v17
	v_cvt_pk_bf16_f32 v3, v3, v4
	ds_write_b64 v216, v[2:3] offset:4096
	s_lshl_b64 s[4:5], s[86:87], 14
	s_ashr_i32 s43, s42, 31
	s_add_u32 s4, s4, s42
	ds_read_b128 v[2:5], v217 offset:4096
	v_mul_lo_u32 v6, s81, v203
	s_addc_u32 s5, s5, s43
	v_ashrrev_i32_e32 v7, 31, v6
	s_lshl_b32 s90, s37, 1
	v_lshl_add_u64 v[6:7], s[4:5], 0, v[6:7]
	v_lshl_add_u64 v[10:11], v[184:185], 0, s[90:91]
	v_lshlrev_b64 v[6:7], 11, v[6:7]
	v_lshl_add_u64 v[12:13], v[10:11], 0, v[6:7]
	ds_read_b128 v[6:9], v218 offset:4096
	s_waitcnt lgkmcnt(0)
	global_store_dwordx4 v[12:13], v[2:5], off
	s_nop 1
	v_mul_lo_u32 v2, s81, v204
	v_ashrrev_i32_e32 v3, 31, v2
	v_lshl_add_u64 v[2:3], s[4:5], 0, v[2:3]
	v_lshlrev_b64 v[2:3], 11, v[2:3]
	v_lshl_add_u64 v[2:3], v[10:11], 0, v[2:3]
	global_store_dwordx4 v[2:3], v[6:9], off
	ds_read_b128 v[2:5], v219 offset:4096
	s_nop 0
	v_mul_lo_u32 v6, s81, v205
	v_ashrrev_i32_e32 v7, 31, v6
	v_lshl_add_u64 v[6:7], s[4:5], 0, v[6:7]
	v_lshlrev_b64 v[6:7], 11, v[6:7]
	v_lshl_add_u64 v[12:13], v[10:11], 0, v[6:7]
	ds_read_b128 v[6:9], v220 offset:4096
	s_waitcnt lgkmcnt(0)
	global_store_dwordx4 v[12:13], v[2:5], off
	s_nop 1
	v_mul_lo_u32 v2, s81, v206
	v_ashrrev_i32_e32 v3, 31, v2
	v_lshl_add_u64 v[2:3], s[4:5], 0, v[2:3]
	v_lshlrev_b64 v[2:3], 11, v[2:3]
	v_lshl_add_u64 v[2:3], v[10:11], 0, v[2:3]
	global_store_dwordx4 v[2:3], v[6:9], off
	s_and_saveexec_b64 s[4:5], s[6:7]
	s_cbranch_execz .LBB0_487
	v_log_f32_e32 v2, v34
	s_lshl_b64 s[44:45], s[86:87], 20
	v_readlane_b32 s37, v254, 17
	v_ashrrev_i32_e32 v181, 31, v180
	v_add_f32_e32 v2, v66, v2
	s_add_u32 s44, s37, s44
	v_readlane_b32 s37, v254, 18
	v_mul_f32_e32 v4, 0x3f317218, v2
	s_addc_u32 s45, s37, s45
	v_lshlrev_b64 v[2:3], 6, v[180:181]
	s_mov_b32 s89, s91
	v_lshl_add_u64 v[2:3], s[44:45], 0, v[2:3]
	v_lshl_add_u64 v[2:3], s[88:89], 2, v[2:3]
	global_store_dword v[2:3], v4, off
.LBB0_487:
	s_or_b64 exec, exec, s[4:5]
	s_waitcnt lgkmcnt(0)
	s_and_b64 vcc, exec, s[72:73]
	s_cbranch_vccnz .LBB0_430
	v_mov_b64_e32 v[146:147], v[174:175]
	v_mov_b64_e32 v[150:151], v[170:171]
	v_mov_b64_e32 v[154:155], v[166:167]
	v_mov_b64_e32 v[158:159], v[162:163]
	v_mov_b64_e32 v[148:149], v[176:177]
	v_mov_b64_e32 v[152:153], v[172:173]
	v_mov_b64_e32 v[156:157], v[168:169]
	v_mov_b64_e32 v[160:161], v[164:165]
	v_mov_b32_e32 v182, v187
	v_mov_b32_e32 v178, v190
	v_mov_b32_e32 v180, v183
	s_mov_b32 s82, s48
	s_mov_b32 s42, s80
	s_mov_b32 s33, s41
	s_mov_b32 s81, s47
	s_mov_b32 s88, s40
	s_mov_b32 s86, s39
	v_and_b32_e32 v2, 63, v0
	v_lshrrev_b32_e32 v3, 3, v2
	v_and_b32_e32 v6, 7, v2
	v_lshlrev_b32_e32 v6, 4, v6
	s_lshl_b32 s4, s88, 7
	s_add_u32 s4, s4, 0x1000
	v_add_u32_e32 v6, s4, v6
	v_mov_b32_e32 v7, 0
	v_lshl_add_u64 v[8:9], s[84:85], 0, v[6:7]
	s_bfe_u32 s5, s75, 0x2000c
	s_and_b32 s43, s75, 0xffff0000
	s_add_u32 s44, s5, 1
	s_lshl_b32 s4, s44, 5
	v_add_u32_e32 v4, s4, v3
	s_lshl_b32 s4, s44, 12
	s_add_u32 s4, s4, s43
	v_mul_lo_u32 v5, v4, s81
	v_add_u32_e32 v5, s82, v5
	v_max_i32_e32 v5, 0, v5
	s_mov_b32 m0, s4
	v_mad_u64_u32 v[10:11], vcc, v5, s21, v[8:9]
	global_load_lds_dwordx4 v[10:11], off
	v_add_u32_e32 v4, 8, v4
	v_mul_lo_u32 v5, v4, s81
	v_add_u32_e32 v5, s82, v5
	v_max_i32_e32 v5, 0, v5
	s_add_u32 m0, s4, 0x400
	v_mad_u64_u32 v[10:11], vcc, v5, s21, v[8:9]
	global_load_lds_dwordx4 v[10:11], off
	v_add_u32_e32 v4, 8, v4
	v_mul_lo_u32 v5, v4, s81
	v_add_u32_e32 v5, s82, v5
	v_max_i32_e32 v5, 0, v5
	s_add_u32 m0, s4, 0x800
	v_mad_u64_u32 v[10:11], vcc, v5, s21, v[8:9]
	global_load_lds_dwordx4 v[10:11], off
	v_add_u32_e32 v4, 8, v4
	v_mul_lo_u32 v5, v4, s81
	v_add_u32_e32 v5, s82, v5
	v_max_i32_e32 v5, 0, v5
	s_add_u32 m0, s4, 0xc00
	v_mad_u64_u32 v[10:11], vcc, v5, s21, v[8:9]
	global_load_lds_dwordx4 v[10:11], off
	s_add_u32 s44, s5, 4
	s_cmp_eq_u32 s5, 0
	s_cselect_b32 s44, 0, s44
	s_lshl_b32 s4, s44, 5
	v_add_u32_e32 v4, s4, v3
	s_lshl_b32 s4, s44, 12
	s_add_u32 s4, s4, s43
	v_mul_lo_u32 v5, v4, s81
	v_add_u32_e32 v5, s82, v5
	v_max_i32_e32 v5, 0, v5
	s_mov_b32 m0, s4
	v_mad_u64_u32 v[10:11], vcc, v5, s21, v[8:9]
	global_load_lds_dwordx4 v[10:11], off
	v_add_u32_e32 v4, 8, v4
	v_mul_lo_u32 v5, v4, s81
	v_add_u32_e32 v5, s82, v5
	v_max_i32_e32 v5, 0, v5
	s_add_u32 m0, s4, 0x400
	v_mad_u64_u32 v[10:11], vcc, v5, s21, v[8:9]
	global_load_lds_dwordx4 v[10:11], off
	v_add_u32_e32 v4, 8, v4
	v_mul_lo_u32 v5, v4, s81
	v_add_u32_e32 v5, s82, v5
	v_max_i32_e32 v5, 0, v5
	s_add_u32 m0, s4, 0x800
	v_mad_u64_u32 v[10:11], vcc, v5, s21, v[8:9]
	global_load_lds_dwordx4 v[10:11], off
	v_add_u32_e32 v4, 8, v4
	v_mul_lo_u32 v5, v4, s81
	v_add_u32_e32 v5, s82, v5
	v_max_i32_e32 v5, 0, v5
	s_add_u32 m0, s4, 0xc00
	v_mad_u64_u32 v[10:11], vcc, v5, s21, v[8:9]
	global_load_lds_dwordx4 v[10:11], off
	s_branch .LBB0_430
